# static priority: one s_setprio 1 for waves 4-7 per GEMM phase, all per-segment flips in the K-loops deleted (strategy lever 4)
# baseline (speedup 1.0000x reference)
; #define PG8_STAGE(bufoff, gbase, voff) do { _Pragma("unroll") for (int _i = 0; _i < 2; ++_i) \
;         __builtin_amdgcn_global_load_lds((const unsigned*)((const char*)(gbase) + (voff)[_i]), (PG8_LAS unsigned*)(lds + (bufoff) + ldsw + _i * 8192), 16, 0, 0); } while (0)
; #define PG8_LDA(dst, b, h) do { _Pragma("unroll") for (int m = 0; m < 4; ++m) _Pragma("unroll") for (int k = 0; k < 2; ++k) dst[m][k] = *(const PG8_LAS bf16x8*)(lds + PG8_SA(b, h) + aoff + m * 2048 + k * 1024); } while (0)
; #define PG8_LDB(dst, b, h) do { _Pragma("unroll") for (int n = 0; n < 2; ++n) _Pragma("unroll") for (int k = 0; k < 2; ++k) dst[n][k] = *(const PG8_LAS bf16x8*)(lds + PG8_SB(b, h) + boff + n * 2048 + k * 1024); } while (0)
; #define PG8_MMA(ai, bj, At, Bt) do { __builtin_amdgcn_s_setprio(1); _Pragma("unroll") for (int m = 0; m < 4; ++m) _Pragma("unroll") for (int n = 0; n < 2; ++n) _Pragma("unroll") for (int k = 0; k < 2; ++k) \
;         acc[ai][bj][m][n] = __builtin_amdgcn_mfma_f32_16x16x32_bf16(Bt[n][k], At[m][k], acc[ai][bj][m][n], 0, 0, 0); __builtin_amdgcn_s_setprio(0); } while (0)
; #define PG8_WAIT_V(n) asm volatile("s_waitcnt vmcnt(" #n ")" ::: "memory")
; #define PG8_BAR __builtin_amdgcn_s_barrier()
; template <class Epi, class Sched, bool ALIGN_EPI>
; __device__ __forceinline__ void gemm_phase(PG8_LAS unsigned char* lds, const Gemm g, const Sched& S, const Epi& E, const int tid) {
;     ...
;         const char* nA = has_next ? (const char*)g.A + (size_t)nxt.pm * tstepA + PG8_ACOL(nxt) : cA; const char* nB = has_next ? (const char*)g.Bt + (size_t)nxt.pn * tstepB : cB;
;         for (int t = 0; t < nt; t += 2) {
;             const bool last = (t == nt - 2);
;             const char* a1 = cA + (size_t)(t + 1) * kstepA;
;             const char* a2 = last ? nA : cA + (size_t)(t + 2) * kstepA; const char* b2 = last ? nB : cB + (size_t)(t + 2) * kstepB;
;             const char* a3 = a2 + kstepA; const char* b3 = b2 + kstepB;
;             if (last && has_next) S.a_ready(nxt);
;             PG8_LDB(B0, 0, 0); PG8_LDB(B1, 0, 1); PG8_SCHED; PG8_LDA(At, 0, 0); PG8_STAGE(PG8_SA(1, 1), a1 + hstepA, voffA);
;             PG8_WAIT_V(8); PG8_WAIT_L(0); PG8_BAR; PG8_MMA(0, 0, At, B0); PG8_MMA(0, 1, At, B1); PG8_BAR; PG8_SCHED;
;             PG8_LDA(At, 0, 1); PG8_STAGE(PG8_SB(0, 0), b2, voffB); PG8_STAGE(PG8_SB(0, 1), b2 + hstepB, voffB); PG8_STAGE(PG8_SA(0, 0), a2, voffA);
.LBB0_245:
	s_ashr_i32 s11, s10, 31
	s_lshl_b64 s[12:13], s[10:11], 20
	s_add_u32 s12, s43, s12
	s_addc_u32 s13, s44, s13
	s_and_b64 s[14:15], s[2:3], exec
	s_cselect_b32 s11, s13, s17
	s_cselect_b32 s58, s12, s16
	s_ashr_i32 s9, s8, 31
	s_lshl_b64 s[14:15], s[8:9], 20
	s_add_u32 s14, s40, s14
	s_addc_u32 s15, s41, s15
	s_and_b64 s[20:21], s[2:3], exec
	s_cselect_b32 s9, s15, s19
	s_cselect_b32 s59, s14, s18
	s_add_u32 s16, s16, 0xc000
	s_addc_u32 s17, s17, 0
	s_add_u32 s60, s18, 0x10000
	s_addc_u32 s61, s19, 0
	s_mov_b32 s62, -2
	v_add_u32_e32 v166, 0x10000, v178
	s_add_u32 s18, s16, 0x4000
	s_addc_u32 s19, s17, 0
	s_cmp_eq_u32 s62, 28
	s_cselect_b32 s22, s58, s18
	s_cselect_b32 s23, s11, s19
	s_cselect_b32 s20, s59, s60
	s_cselect_b32 s21, s9, s61
	s_add_u32 s18, s22, 0x8000
	s_addc_u32 s19, s23, 0
	s_add_i32 s63, 0, 0x10000
	s_add_i32 s66, 0, 0x14000
	ds_read_b128 v[80:83], v166
	ds_read_b128 v[84:87], v166 offset:1024
	ds_read_b128 v[96:99], v166 offset:2048
	ds_read_b128 v[100:103], v166 offset:3072
	ds_read_b128 v[162:165], v166 offset:16384
	ds_read_b128 v[182:185], v166 offset:17408
	ds_read_b128 v[186:189], v166 offset:18432
	ds_read_b128 v[190:193], v166 offset:19456
	s_add_i32 m0, s45, 0xc000
	ds_read_b128 v[194:197], v180
	ds_read_b128 v[198:201], v180 offset:1024
	ds_read_b128 v[202:205], v180 offset:2048
	ds_read_b128 v[206:209], v180 offset:3072
	ds_read_b128 v[210:213], v180 offset:4096
	ds_read_b128 v[214:217], v180 offset:5120
	ds_read_b128 v[218:221], v180 offset:6144
	ds_read_b128 v[222:225], v180 offset:7168
	global_load_lds_dwordx4 v158, s[16:17]
	s_add_i32 m0, s45, 0xe000
	s_nop 0
	global_load_lds_dwordx4 v160, s[16:17]
	s_waitcnt vmcnt(8)
	s_waitcnt lgkmcnt(0)
	s_and_b64 vcc, exec, s[6:7]
	s_cbranch_vccnz .Lsprio_0
	s_setprio 1
.Lsprio_0:
	s_barrier
	v_mfma_f32_16x16x32_bf16 v[142:145], v[80:83], v[194:197], 0
	v_mfma_f32_16x16x32_bf16 v[134:137], v[96:99], v[194:197], 0
	v_mfma_f32_16x16x32_bf16 v[124:127], v[80:83], v[202:205], 0
	v_mfma_f32_16x16x32_bf16 v[116:119], v[96:99], v[202:205], 0
	v_mfma_f32_16x16x32_bf16 v[108:111], v[80:83], v[210:213], 0
	v_mfma_f32_16x16x32_bf16 v[92:95], v[96:99], v[210:213], 0
	v_mfma_f32_16x16x32_bf16 v[76:79], v[80:83], v[218:221], 0
	v_mfma_f32_16x16x32_bf16 v[68:71], v[96:99], v[218:221], 0
	v_mfma_f32_16x16x32_bf16 v[142:145], v[84:87], v[198:201], v[142:145]
	v_mfma_f32_16x16x32_bf16 v[134:137], v[100:103], v[198:201], v[134:137]
	v_mfma_f32_16x16x32_bf16 v[124:127], v[84:87], v[206:209], v[124:127]
	v_mfma_f32_16x16x32_bf16 v[116:119], v[100:103], v[206:209], v[116:119]
	v_mfma_f32_16x16x32_bf16 v[108:111], v[84:87], v[214:217], v[108:111]
	v_mfma_f32_16x16x32_bf16 v[92:95], v[100:103], v[214:217], v[92:95]
	v_mfma_f32_16x16x32_bf16 v[76:79], v[84:87], v[222:225], v[76:79]
	v_mfma_f32_16x16x32_bf16 v[68:71], v[100:103], v[222:225], v[68:71]
	v_mfma_f32_16x16x32_bf16 v[138:141], v[162:165], v[194:197], 0
	v_mfma_f32_16x16x32_bf16 v[130:133], v[186:189], v[194:197], 0
	v_mfma_f32_16x16x32_bf16 v[120:123], v[162:165], v[202:205], 0
	v_mfma_f32_16x16x32_bf16 v[112:115], v[186:189], v[202:205], 0
	v_mfma_f32_16x16x32_bf16 v[104:107], v[162:165], v[210:213], 0
	v_mfma_f32_16x16x32_bf16 v[88:91], v[186:189], v[210:213], 0
	v_mfma_f32_16x16x32_bf16 v[72:75], v[162:165], v[218:221], 0
	v_mfma_f32_16x16x32_bf16 v[64:67], v[186:189], v[218:221], 0
	v_mfma_f32_16x16x32_bf16 v[138:141], v[182:185], v[198:201], v[138:141]
	v_mfma_f32_16x16x32_bf16 v[130:133], v[190:193], v[198:201], v[130:133]
	v_mfma_f32_16x16x32_bf16 v[120:123], v[182:185], v[206:209], v[120:123]
	v_mfma_f32_16x16x32_bf16 v[112:115], v[190:193], v[206:209], v[112:115]
	v_mfma_f32_16x16x32_bf16 v[104:107], v[182:185], v[214:217], v[104:107]
	v_mfma_f32_16x16x32_bf16 v[88:91], v[190:193], v[214:217], v[88:91]
	v_mfma_f32_16x16x32_bf16 v[72:75], v[182:185], v[222:225], v[72:75]
	v_mfma_f32_16x16x32_bf16 v[64:67], v[190:193], v[222:225], v[64:67]
	s_barrier
	s_add_i32 s63, s63, s42
	s_mov_b32 m0, s63
	ds_read_b128 v[194:197], v180 offset:16384
	ds_read_b128 v[198:201], v180 offset:17408
	ds_read_b128 v[202:205], v180 offset:18432
	ds_read_b128 v[206:209], v180 offset:19456
	ds_read_b128 v[210:213], v180 offset:20480
	ds_read_b128 v[214:217], v180 offset:21504
	ds_read_b128 v[218:221], v180 offset:22528
	ds_read_b128 v[222:225], v180 offset:23552
	global_load_lds_dwordx4 v150, s[20:21]
	s_add_i32 m0, s63, 0x2000
	s_add_u32 s64, s20, 0x4000
	s_addc_u32 s65, s21, 0
	s_add_i32 s63, s66, s42
	global_load_lds_dwordx4 v146, s[20:21]
	s_mov_b32 m0, s63
	s_nop 0
	global_load_lds_dwordx4 v150, s[64:65]
	s_add_i32 m0, s63, 0x2000
	s_nop 0
	global_load_lds_dwordx4 v146, s[64:65]
	s_mov_b32 m0, s45
	s_nop 0
	global_load_lds_dwordx4 v152, s[22:23]
	s_mov_b32 m0, s46
	s_nop 0
	global_load_lds_dwordx4 v148, s[22:23]
	s_waitcnt vmcnt(8)
	s_waitcnt lgkmcnt(0)
	s_barrier
; #define PG8_STAGE(bufoff, gbase, voff) do { _Pragma("unroll") for (int _i = 0; _i < 2; ++_i) \
;         __builtin_amdgcn_global_load_lds((const unsigned*)((const char*)(gbase) + (voff)[_i]), (PG8_LAS unsigned*)(lds + (bufoff) + ldsw + _i * 8192), 16, 0, 0); } while (0)
; #define PG8_LDA(dst, b, h) do { _Pragma("unroll") for (int m = 0; m < 4; ++m) _Pragma("unroll") for (int k = 0; k < 2; ++k) dst[m][k] = *(const PG8_LAS bf16x8*)(lds + PG8_SA(b, h) + aoff + m * 2048 + k * 1024); } while (0)
; #define PG8_LDB(dst, b, h) do { _Pragma("unroll") for (int n = 0; n < 2; ++n) _Pragma("unroll") for (int k = 0; k < 2; ++k) dst[n][k] = *(const PG8_LAS bf16x8*)(lds + PG8_SB(b, h) + boff + n * 2048 + k * 1024); } while (0)
; #define PG8_MMA(ai, bj, At, Bt) do { __builtin_amdgcn_s_setprio(1); _Pragma("unroll") for (int m = 0; m < 4; ++m) _Pragma("unroll") for (int n = 0; n < 2; ++n) _Pragma("unroll") for (int k = 0; k < 2; ++k) \
;         acc[ai][bj][m][n] = __builtin_amdgcn_mfma_f32_16x16x32_bf16(Bt[n][k], At[m][k], acc[ai][bj][m][n], 0, 0, 0); __builtin_amdgcn_s_setprio(0); } while (0)
; #define PG8_WAIT_V(n) asm volatile("s_waitcnt vmcnt(" #n ")" ::: "memory")
; #define PG8_WAIT_L(n) asm volatile("s_waitcnt lgkmcnt(" #n ")" ::: "memory")
; #define PG8_BAR __builtin_amdgcn_s_barrier()
; #define PG8_SCHED __builtin_amdgcn_sched_barrier(0)
; template <class Epi, class Sched, bool ALIGN_EPI>
; __device__ __forceinline__ void gemm_phase(PG8_LAS unsigned char* lds, const Gemm g, const Sched& S, const Epi& E, const int tid) {
;     ...
;             PG8_WAIT_V(8); PG8_WAIT_L(0); PG8_BAR; PG8_MMA(1, 0, At, B0); PG8_MMA(1, 1, At, B1); PG8_BAR; PG8_SCHED;
;             PG8_LDB(B0, 1, 0); PG8_LDB(B1, 1, 1); PG8_SCHED; PG8_LDA(At, 1, 0); PG8_STAGE(PG8_SA(0, 1), a2 + hstepA, voffA);
;             PG8_WAIT_V(8); PG8_WAIT_L(0); PG8_BAR; PG8_MMA(0, 0, At, B0); PG8_MMA(0, 1, At, B1); PG8_BAR; PG8_SCHED;
;             PG8_LDA(At, 1, 1); PG8_STAGE(PG8_SB(1, 0), b3, voffB); PG8_STAGE(PG8_SB(1, 1), b3 + hstepB, voffB); PG8_STAGE(PG8_SA(1, 0), a3, voffA);
	v_mfma_f32_16x16x32_bf16 v[60:63], v[80:83], v[194:197], 0
	v_mfma_f32_16x16x32_bf16 v[52:55], v[96:99], v[194:197], 0
	v_mfma_f32_16x16x32_bf16 v[44:47], v[80:83], v[202:205], 0
	v_mfma_f32_16x16x32_bf16 v[36:39], v[96:99], v[202:205], 0
	v_mfma_f32_16x16x32_bf16 v[28:31], v[80:83], v[210:213], 0
	v_mfma_f32_16x16x32_bf16 v[20:23], v[96:99], v[210:213], 0
	v_mfma_f32_16x16x32_bf16 v[12:15], v[80:83], v[218:221], 0
	v_mfma_f32_16x16x32_bf16 v[4:7], v[96:99], v[218:221], 0
	v_mfma_f32_16x16x32_bf16 v[60:63], v[84:87], v[198:201], v[60:63]
	v_mfma_f32_16x16x32_bf16 v[52:55], v[100:103], v[198:201], v[52:55]
	v_mfma_f32_16x16x32_bf16 v[44:47], v[84:87], v[206:209], v[44:47]
	v_mfma_f32_16x16x32_bf16 v[36:39], v[100:103], v[206:209], v[36:39]
	v_mfma_f32_16x16x32_bf16 v[28:31], v[84:87], v[214:217], v[28:31]
	v_mfma_f32_16x16x32_bf16 v[20:23], v[100:103], v[214:217], v[20:23]
	v_mfma_f32_16x16x32_bf16 v[12:15], v[84:87], v[222:225], v[12:15]
	v_mfma_f32_16x16x32_bf16 v[4:7], v[100:103], v[222:225], v[4:7]
	v_mfma_f32_16x16x32_bf16 v[56:59], v[162:165], v[194:197], 0
	v_mfma_f32_16x16x32_bf16 v[48:51], v[186:189], v[194:197], 0
	v_mfma_f32_16x16x32_bf16 v[40:43], v[162:165], v[202:205], 0
	v_mfma_f32_16x16x32_bf16 v[32:35], v[186:189], v[202:205], 0
	v_mfma_f32_16x16x32_bf16 v[24:27], v[162:165], v[210:213], 0
	v_mfma_f32_16x16x32_bf16 v[16:19], v[186:189], v[210:213], 0
	v_mfma_f32_16x16x32_bf16 v[8:11], v[162:165], v[218:221], 0
	v_mfma_f32_16x16x32_bf16 v[0:3], v[186:189], v[218:221], 0
	v_mfma_f32_16x16x32_bf16 v[56:59], v[182:185], v[198:201], v[56:59]
	v_mfma_f32_16x16x32_bf16 v[48:51], v[190:193], v[198:201], v[48:51]
	v_mfma_f32_16x16x32_bf16 v[40:43], v[182:185], v[206:209], v[40:43]
	v_mfma_f32_16x16x32_bf16 v[32:35], v[190:193], v[206:209], v[32:35]
	v_mfma_f32_16x16x32_bf16 v[24:27], v[182:185], v[214:217], v[24:27]
	v_mfma_f32_16x16x32_bf16 v[16:19], v[190:193], v[214:217], v[16:19]
	v_mfma_f32_16x16x32_bf16 v[8:11], v[182:185], v[222:225], v[8:11]
	v_mfma_f32_16x16x32_bf16 v[0:3], v[190:193], v[222:225], v[0:3]
	s_barrier
	s_add_i32 s63, 0, 0x18000
	s_add_i32 s64, 0, 0x1c000
	ds_read_b128 v[80:83], v166 offset:32768
	ds_read_b128 v[84:87], v166 offset:33792
	ds_read_b128 v[96:99], v166 offset:34816
	ds_read_b128 v[100:103], v166 offset:35840
	ds_read_b128 v[162:165], v166 offset:49152
	ds_read_b128 v[182:185], v166 offset:50176
	ds_read_b128 v[186:189], v166 offset:51200
	ds_read_b128 v[190:193], v166 offset:52224
	s_add_u32 s22, s22, 0x4000
	s_addc_u32 s23, s23, 0
	s_mov_b32 m0, s47
	ds_read_b128 v[194:197], v180 offset:32768
	ds_read_b128 v[198:201], v180 offset:33792
	ds_read_b128 v[202:205], v180 offset:34816
	ds_read_b128 v[206:209], v180 offset:35840
	ds_read_b128 v[210:213], v180 offset:36864
	ds_read_b128 v[214:217], v180 offset:37888
	ds_read_b128 v[218:221], v180 offset:38912
	ds_read_b128 v[222:225], v180 offset:39936
	global_load_lds_dwordx4 v152, s[22:23]
	s_mov_b32 m0, s48
	s_nop 0
	global_load_lds_dwordx4 v148, s[22:23]
	s_waitcnt vmcnt(8)
	s_waitcnt lgkmcnt(0)
	s_barrier
	v_mfma_f32_16x16x32_bf16 v[142:145], v[80:83], v[194:197], v[142:145]
	v_mfma_f32_16x16x32_bf16 v[134:137], v[96:99], v[194:197], v[134:137]
	v_mfma_f32_16x16x32_bf16 v[124:127], v[80:83], v[202:205], v[124:127]
	v_mfma_f32_16x16x32_bf16 v[116:119], v[96:99], v[202:205], v[116:119]
	v_mfma_f32_16x16x32_bf16 v[108:111], v[80:83], v[210:213], v[108:111]
	v_mfma_f32_16x16x32_bf16 v[92:95], v[96:99], v[210:213], v[92:95]
	v_mfma_f32_16x16x32_bf16 v[76:79], v[80:83], v[218:221], v[76:79]
	v_mfma_f32_16x16x32_bf16 v[68:71], v[96:99], v[218:221], v[68:71]
	v_mfma_f32_16x16x32_bf16 v[142:145], v[84:87], v[198:201], v[142:145]
	v_mfma_f32_16x16x32_bf16 v[134:137], v[100:103], v[198:201], v[134:137]
	v_mfma_f32_16x16x32_bf16 v[124:127], v[84:87], v[206:209], v[124:127]
	v_mfma_f32_16x16x32_bf16 v[116:119], v[100:103], v[206:209], v[116:119]
	v_mfma_f32_16x16x32_bf16 v[108:111], v[84:87], v[214:217], v[108:111]
	v_mfma_f32_16x16x32_bf16 v[92:95], v[100:103], v[214:217], v[92:95]
	v_mfma_f32_16x16x32_bf16 v[76:79], v[84:87], v[222:225], v[76:79]
	v_mfma_f32_16x16x32_bf16 v[68:71], v[100:103], v[222:225], v[68:71]
	v_mfma_f32_16x16x32_bf16 v[138:141], v[162:165], v[194:197], v[138:141]
	v_mfma_f32_16x16x32_bf16 v[130:133], v[186:189], v[194:197], v[130:133]
	v_mfma_f32_16x16x32_bf16 v[120:123], v[162:165], v[202:205], v[120:123]
	v_mfma_f32_16x16x32_bf16 v[112:115], v[186:189], v[202:205], v[112:115]
	v_mfma_f32_16x16x32_bf16 v[104:107], v[162:165], v[210:213], v[104:107]
	v_mfma_f32_16x16x32_bf16 v[88:91], v[186:189], v[210:213], v[88:91]
	v_mfma_f32_16x16x32_bf16 v[72:75], v[162:165], v[218:221], v[72:75]
	v_mfma_f32_16x16x32_bf16 v[64:67], v[186:189], v[218:221], v[64:67]
	v_mfma_f32_16x16x32_bf16 v[138:141], v[182:185], v[198:201], v[138:141]
	v_mfma_f32_16x16x32_bf16 v[130:133], v[190:193], v[198:201], v[130:133]
	v_mfma_f32_16x16x32_bf16 v[120:123], v[182:185], v[206:209], v[120:123]
	v_mfma_f32_16x16x32_bf16 v[112:115], v[190:193], v[206:209], v[112:115]
	v_mfma_f32_16x16x32_bf16 v[104:107], v[182:185], v[214:217], v[104:107]
	v_mfma_f32_16x16x32_bf16 v[88:91], v[190:193], v[214:217], v[88:91]
	v_mfma_f32_16x16x32_bf16 v[72:75], v[182:185], v[222:225], v[72:75]
	v_mfma_f32_16x16x32_bf16 v[64:67], v[190:193], v[222:225], v[64:67]
	s_barrier
; #define PG8_STAGE(bufoff, gbase, voff) do { _Pragma("unroll") for (int _i = 0; _i < 2; ++_i) \
;         __builtin_amdgcn_global_load_lds((const unsigned*)((const char*)(gbase) + (voff)[_i]), (PG8_LAS unsigned*)(lds + (bufoff) + ldsw + _i * 8192), 16, 0, 0); } while (0)
; #define PG8_LDA(dst, b, h) do { _Pragma("unroll") for (int m = 0; m < 4; ++m) _Pragma("unroll") for (int k = 0; k < 2; ++k) dst[m][k] = *(const PG8_LAS bf16x8*)(lds + PG8_SA(b, h) + aoff + m * 2048 + k * 1024); } while (0)
; #define PG8_LDB(dst, b, h) do { _Pragma("unroll") for (int n = 0; n < 2; ++n) _Pragma("unroll") for (int k = 0; k < 2; ++k) dst[n][k] = *(const PG8_LAS bf16x8*)(lds + PG8_SB(b, h) + boff + n * 2048 + k * 1024); } while (0)
; #define PG8_MMA(ai, bj, At, Bt) do { __builtin_amdgcn_s_setprio(1); _Pragma("unroll") for (int m = 0; m < 4; ++m) _Pragma("unroll") for (int n = 0; n < 2; ++n) _Pragma("unroll") for (int k = 0; k < 2; ++k) \
;         acc[ai][bj][m][n] = __builtin_amdgcn_mfma_f32_16x16x32_bf16(Bt[n][k], At[m][k], acc[ai][bj][m][n], 0, 0, 0); __builtin_amdgcn_s_setprio(0); } while (0)
; #define PG8_WAIT_V(n) asm volatile("s_waitcnt vmcnt(" #n ")" ::: "memory")
; #define PG8_WAIT_L(n) asm volatile("s_waitcnt lgkmcnt(" #n ")" ::: "memory")
; #define PG8_BAR __builtin_amdgcn_s_barrier()
; #define PG8_SCHED __builtin_amdgcn_sched_barrier(0)
; template <class Epi, class Sched, bool ALIGN_EPI>
; __device__ __forceinline__ void gemm_phase(PG8_LAS unsigned char* lds, const Gemm g, const Sched& S, const Epi& E, const int tid) {
;     ...
;             PG8_LDB(B0, 0, 0); PG8_LDB(B1, 0, 1); PG8_SCHED; PG8_LDA(At, 0, 0); PG8_STAGE(PG8_SA(1, 1), a1 + hstepA, voffA);
;             PG8_WAIT_V(8); PG8_WAIT_L(0); PG8_BAR; PG8_MMA(0, 0, At, B0); PG8_MMA(0, 1, At, B1); PG8_BAR; PG8_SCHED;
;     ...
;             PG8_LDA(At, 1, 1); PG8_STAGE(PG8_SB(1, 0), b3, voffB); PG8_STAGE(PG8_SB(1, 1), b3 + hstepB, voffB); PG8_STAGE(PG8_SA(1, 0), a3, voffA);
;             PG8_WAIT_V(8); PG8_WAIT_L(0); PG8_BAR; PG8_MMA(1, 0, At, B0); PG8_MMA(1, 1, At, B1); PG8_BAR; PG8_SCHED;
	s_add_u32 s22, s20, 0x8000
	s_addc_u32 s23, s21, 0
	s_add_i32 s63, s63, s42
	s_mov_b32 m0, s63
	ds_read_b128 v[194:197], v180 offset:49152
	ds_read_b128 v[198:201], v180 offset:50176
	ds_read_b128 v[202:205], v180 offset:51200
	ds_read_b128 v[206:209], v180 offset:52224
	ds_read_b128 v[210:213], v180 offset:53248
	ds_read_b128 v[214:217], v180 offset:54272
	ds_read_b128 v[218:221], v180 offset:55296
	ds_read_b128 v[222:225], v180 offset:56320
	global_load_lds_dwordx4 v150, s[22:23]
	s_add_i32 m0, s63, 0x2000
	s_add_u32 s20, s20, 0xc000
	s_addc_u32 s21, s21, 0
	global_load_lds_dwordx4 v146, s[22:23]
	s_add_i32 s22, s64, s42
	s_mov_b32 m0, s22
	s_nop 0
	global_load_lds_dwordx4 v150, s[20:21]
	s_add_i32 m0, s22, 0x2000
	s_nop 0
	global_load_lds_dwordx4 v146, s[20:21]
	s_mov_b32 m0, s51
	s_nop 0
	global_load_lds_dwordx4 v152, s[18:19]
	s_mov_b32 m0, s52
	s_nop 0
	global_load_lds_dwordx4 v148, s[18:19]
	s_waitcnt vmcnt(8)
	s_waitcnt lgkmcnt(0)
	s_barrier
	v_mfma_f32_16x16x32_bf16 v[60:63], v[80:83], v[194:197], v[60:63]
	v_mfma_f32_16x16x32_bf16 v[52:55], v[96:99], v[194:197], v[52:55]
	v_mfma_f32_16x16x32_bf16 v[44:47], v[80:83], v[202:205], v[44:47]
	v_mfma_f32_16x16x32_bf16 v[36:39], v[96:99], v[202:205], v[36:39]
	v_mfma_f32_16x16x32_bf16 v[28:31], v[80:83], v[210:213], v[28:31]
	v_mfma_f32_16x16x32_bf16 v[20:23], v[96:99], v[210:213], v[20:23]
	v_mfma_f32_16x16x32_bf16 v[12:15], v[80:83], v[218:221], v[12:15]
	v_mfma_f32_16x16x32_bf16 v[4:7], v[96:99], v[218:221], v[4:7]
	v_mfma_f32_16x16x32_bf16 v[60:63], v[84:87], v[198:201], v[60:63]
	v_mfma_f32_16x16x32_bf16 v[52:55], v[100:103], v[198:201], v[52:55]
	v_mfma_f32_16x16x32_bf16 v[44:47], v[84:87], v[206:209], v[44:47]
	v_mfma_f32_16x16x32_bf16 v[36:39], v[100:103], v[206:209], v[36:39]
	v_mfma_f32_16x16x32_bf16 v[28:31], v[84:87], v[214:217], v[28:31]
	v_mfma_f32_16x16x32_bf16 v[20:23], v[100:103], v[214:217], v[20:23]
	v_mfma_f32_16x16x32_bf16 v[12:15], v[84:87], v[222:225], v[12:15]
	v_mfma_f32_16x16x32_bf16 v[4:7], v[100:103], v[222:225], v[4:7]
	v_mfma_f32_16x16x32_bf16 v[56:59], v[162:165], v[194:197], v[56:59]
	v_mfma_f32_16x16x32_bf16 v[48:51], v[186:189], v[194:197], v[48:51]
	v_mfma_f32_16x16x32_bf16 v[40:43], v[162:165], v[202:205], v[40:43]
	v_mfma_f32_16x16x32_bf16 v[32:35], v[186:189], v[202:205], v[32:35]
	v_mfma_f32_16x16x32_bf16 v[24:27], v[162:165], v[210:213], v[24:27]
	v_mfma_f32_16x16x32_bf16 v[16:19], v[186:189], v[210:213], v[16:19]
	v_mfma_f32_16x16x32_bf16 v[8:11], v[162:165], v[218:221], v[8:11]
	v_mfma_f32_16x16x32_bf16 v[0:3], v[186:189], v[218:221], v[0:3]
	v_mfma_f32_16x16x32_bf16 v[56:59], v[182:185], v[198:201], v[56:59]
	v_mfma_f32_16x16x32_bf16 v[48:51], v[190:193], v[198:201], v[48:51]
	v_mfma_f32_16x16x32_bf16 v[40:43], v[182:185], v[206:209], v[40:43]
	v_mfma_f32_16x16x32_bf16 v[32:35], v[190:193], v[206:209], v[32:35]
	v_mfma_f32_16x16x32_bf16 v[24:27], v[182:185], v[214:217], v[24:27]
	v_mfma_f32_16x16x32_bf16 v[16:19], v[190:193], v[214:217], v[16:19]
	v_mfma_f32_16x16x32_bf16 v[8:11], v[182:185], v[222:225], v[8:11]
	v_mfma_f32_16x16x32_bf16 v[0:3], v[190:193], v[222:225], v[0:3]
	s_barrier
	s_add_i32 s62, s62, 2
	s_add_u32 s16, s16, 0x10000
	s_addc_u32 s17, s17, 0
	s_add_u32 s60, s60, 0x10000
	s_addc_u32 s61, s61, 0
.LBB0_246:
	s_add_u32 s18, s16, 0x4000
	s_addc_u32 s19, s17, 0
	s_cmp_eq_u32 s62, 28
	s_cselect_b32 s22, s58, s18
	s_cselect_b32 s23, s11, s19
	s_cselect_b32 s20, s59, s60
	s_cselect_b32 s21, s9, s61
	s_add_u32 s18, s22, 0x8000
	s_addc_u32 s19, s23, 0
	s_add_i32 s63, 0, 0x10000
	s_add_i32 s66, 0, 0x14000
	ds_read_b128 v[80:83], v166
	ds_read_b128 v[84:87], v166 offset:1024
	ds_read_b128 v[96:99], v166 offset:2048
	ds_read_b128 v[100:103], v166 offset:3072
	ds_read_b128 v[162:165], v166 offset:16384
	ds_read_b128 v[182:185], v166 offset:17408
	ds_read_b128 v[186:189], v166 offset:18432
	ds_read_b128 v[190:193], v166 offset:19456
	s_add_i32 m0, s45, 0xc000
	ds_read_b128 v[194:197], v180
	ds_read_b128 v[198:201], v180 offset:1024
	ds_read_b128 v[202:205], v180 offset:2048
	ds_read_b128 v[206:209], v180 offset:3072
	ds_read_b128 v[210:213], v180 offset:4096
	ds_read_b128 v[214:217], v180 offset:5120
	ds_read_b128 v[218:221], v180 offset:6144
	ds_read_b128 v[222:225], v180 offset:7168
	global_load_lds_dwordx4 v158, s[16:17]
	s_add_i32 m0, s45, 0xe000
	s_nop 0
	global_load_lds_dwordx4 v160, s[16:17]
	s_waitcnt vmcnt(8)
	s_waitcnt lgkmcnt(0)
	s_barrier
	v_mfma_f32_16x16x32_bf16 v[142:145], v[80:83], v[194:197], v[142:145]
	v_mfma_f32_16x16x32_bf16 v[134:137], v[96:99], v[194:197], v[134:137]
	v_mfma_f32_16x16x32_bf16 v[124:127], v[80:83], v[202:205], v[124:127]
	v_mfma_f32_16x16x32_bf16 v[116:119], v[96:99], v[202:205], v[116:119]
	v_mfma_f32_16x16x32_bf16 v[108:111], v[80:83], v[210:213], v[108:111]
	v_mfma_f32_16x16x32_bf16 v[92:95], v[96:99], v[210:213], v[92:95]
	v_mfma_f32_16x16x32_bf16 v[76:79], v[80:83], v[218:221], v[76:79]
	v_mfma_f32_16x16x32_bf16 v[68:71], v[96:99], v[218:221], v[68:71]
	v_mfma_f32_16x16x32_bf16 v[142:145], v[84:87], v[198:201], v[142:145]
	v_mfma_f32_16x16x32_bf16 v[134:137], v[100:103], v[198:201], v[134:137]
	v_mfma_f32_16x16x32_bf16 v[124:127], v[84:87], v[206:209], v[124:127]
	v_mfma_f32_16x16x32_bf16 v[116:119], v[100:103], v[206:209], v[116:119]
	v_mfma_f32_16x16x32_bf16 v[108:111], v[84:87], v[214:217], v[108:111]
	v_mfma_f32_16x16x32_bf16 v[92:95], v[100:103], v[214:217], v[92:95]
	v_mfma_f32_16x16x32_bf16 v[76:79], v[84:87], v[222:225], v[76:79]
	v_mfma_f32_16x16x32_bf16 v[68:71], v[100:103], v[222:225], v[68:71]
	v_mfma_f32_16x16x32_bf16 v[138:141], v[162:165], v[194:197], v[138:141]
	v_mfma_f32_16x16x32_bf16 v[130:133], v[186:189], v[194:197], v[130:133]
	v_mfma_f32_16x16x32_bf16 v[120:123], v[162:165], v[202:205], v[120:123]
	v_mfma_f32_16x16x32_bf16 v[112:115], v[186:189], v[202:205], v[112:115]
	v_mfma_f32_16x16x32_bf16 v[104:107], v[162:165], v[210:213], v[104:107]
	v_mfma_f32_16x16x32_bf16 v[88:91], v[186:189], v[210:213], v[88:91]
	v_mfma_f32_16x16x32_bf16 v[72:75], v[162:165], v[218:221], v[72:75]
	v_mfma_f32_16x16x32_bf16 v[64:67], v[186:189], v[218:221], v[64:67]
	v_mfma_f32_16x16x32_bf16 v[138:141], v[182:185], v[198:201], v[138:141]
	v_mfma_f32_16x16x32_bf16 v[130:133], v[190:193], v[198:201], v[130:133]
	v_mfma_f32_16x16x32_bf16 v[120:123], v[182:185], v[206:209], v[120:123]
	v_mfma_f32_16x16x32_bf16 v[112:115], v[190:193], v[206:209], v[112:115]
	v_mfma_f32_16x16x32_bf16 v[104:107], v[182:185], v[214:217], v[104:107]
	v_mfma_f32_16x16x32_bf16 v[88:91], v[190:193], v[214:217], v[88:91]
	v_mfma_f32_16x16x32_bf16 v[72:75], v[182:185], v[222:225], v[72:75]
	v_mfma_f32_16x16x32_bf16 v[64:67], v[190:193], v[222:225], v[64:67]
	s_barrier
; #define PG8_STAGE(bufoff, gbase, voff) do { _Pragma("unroll") for (int _i = 0; _i < 2; ++_i) \
;         __builtin_amdgcn_global_load_lds((const unsigned*)((const char*)(gbase) + (voff)[_i]), (PG8_LAS unsigned*)(lds + (bufoff) + ldsw + _i * 8192), 16, 0, 0); } while (0)
; #define PG8_LDA(dst, b, h) do { _Pragma("unroll") for (int m = 0; m < 4; ++m) _Pragma("unroll") for (int k = 0; k < 2; ++k) dst[m][k] = *(const PG8_LAS bf16x8*)(lds + PG8_SA(b, h) + aoff + m * 2048 + k * 1024); } while (0)
; #define PG8_LDB(dst, b, h) do { _Pragma("unroll") for (int n = 0; n < 2; ++n) _Pragma("unroll") for (int k = 0; k < 2; ++k) dst[n][k] = *(const PG8_LAS bf16x8*)(lds + PG8_SB(b, h) + boff + n * 2048 + k * 1024); } while (0)
; #define PG8_MMA(ai, bj, At, Bt) do { __builtin_amdgcn_s_setprio(1); _Pragma("unroll") for (int m = 0; m < 4; ++m) _Pragma("unroll") for (int n = 0; n < 2; ++n) _Pragma("unroll") for (int k = 0; k < 2; ++k) \
;         acc[ai][bj][m][n] = __builtin_amdgcn_mfma_f32_16x16x32_bf16(Bt[n][k], At[m][k], acc[ai][bj][m][n], 0, 0, 0); __builtin_amdgcn_s_setprio(0); } while (0)
; #define PG8_WAIT_V(n) asm volatile("s_waitcnt vmcnt(" #n ")" ::: "memory")
; #define PG8_WAIT_L(n) asm volatile("s_waitcnt lgkmcnt(" #n ")" ::: "memory")
; #define PG8_BAR __builtin_amdgcn_s_barrier()
; #define PG8_SCHED __builtin_amdgcn_sched_barrier(0)
; template <class Epi, class Sched, bool ALIGN_EPI>
; __device__ __forceinline__ void gemm_phase(PG8_LAS unsigned char* lds, const Gemm g, const Sched& S, const Epi& E, const int tid) {
;     ...
;             PG8_LDA(At, 0, 1); PG8_STAGE(PG8_SB(0, 0), b2, voffB); PG8_STAGE(PG8_SB(0, 1), b2 + hstepB, voffB); PG8_STAGE(PG8_SA(0, 0), a2, voffA);
;             PG8_WAIT_V(8); PG8_WAIT_L(0); PG8_BAR; PG8_MMA(1, 0, At, B0); PG8_MMA(1, 1, At, B1); PG8_BAR; PG8_SCHED;
;             PG8_LDB(B0, 1, 0); PG8_LDB(B1, 1, 1); PG8_SCHED; PG8_LDA(At, 1, 0); PG8_STAGE(PG8_SA(0, 1), a2 + hstepA, voffA);
	s_add_i32 s63, s63, s42
	s_mov_b32 m0, s63
	ds_read_b128 v[194:197], v180 offset:16384
	ds_read_b128 v[198:201], v180 offset:17408
	ds_read_b128 v[202:205], v180 offset:18432
	ds_read_b128 v[206:209], v180 offset:19456
	ds_read_b128 v[210:213], v180 offset:20480
	ds_read_b128 v[214:217], v180 offset:21504
	ds_read_b128 v[218:221], v180 offset:22528
	ds_read_b128 v[222:225], v180 offset:23552
	global_load_lds_dwordx4 v150, s[20:21]
	s_add_i32 m0, s63, 0x2000
	s_add_u32 s64, s20, 0x4000
	s_addc_u32 s65, s21, 0
	s_add_i32 s63, s66, s42
	global_load_lds_dwordx4 v146, s[20:21]
	s_mov_b32 m0, s63
	s_nop 0
	global_load_lds_dwordx4 v150, s[64:65]
	s_add_i32 m0, s63, 0x2000
	s_nop 0
	global_load_lds_dwordx4 v146, s[64:65]
	s_mov_b32 m0, s45
	s_nop 0
	global_load_lds_dwordx4 v152, s[22:23]
	s_mov_b32 m0, s46
	s_nop 0
	global_load_lds_dwordx4 v148, s[22:23]
	s_waitcnt vmcnt(8)
	s_waitcnt lgkmcnt(0)
	s_barrier
	v_mfma_f32_16x16x32_bf16 v[60:63], v[80:83], v[194:197], v[60:63]
	v_mfma_f32_16x16x32_bf16 v[52:55], v[96:99], v[194:197], v[52:55]
	v_mfma_f32_16x16x32_bf16 v[44:47], v[80:83], v[202:205], v[44:47]
	v_mfma_f32_16x16x32_bf16 v[36:39], v[96:99], v[202:205], v[36:39]
	v_mfma_f32_16x16x32_bf16 v[28:31], v[80:83], v[210:213], v[28:31]
	v_mfma_f32_16x16x32_bf16 v[20:23], v[96:99], v[210:213], v[20:23]
	v_mfma_f32_16x16x32_bf16 v[12:15], v[80:83], v[218:221], v[12:15]
	v_mfma_f32_16x16x32_bf16 v[4:7], v[96:99], v[218:221], v[4:7]
	v_mfma_f32_16x16x32_bf16 v[60:63], v[84:87], v[198:201], v[60:63]
	v_mfma_f32_16x16x32_bf16 v[52:55], v[100:103], v[198:201], v[52:55]
	v_mfma_f32_16x16x32_bf16 v[44:47], v[84:87], v[206:209], v[44:47]
	v_mfma_f32_16x16x32_bf16 v[36:39], v[100:103], v[206:209], v[36:39]
	v_mfma_f32_16x16x32_bf16 v[28:31], v[84:87], v[214:217], v[28:31]
	v_mfma_f32_16x16x32_bf16 v[20:23], v[100:103], v[214:217], v[20:23]
	v_mfma_f32_16x16x32_bf16 v[12:15], v[84:87], v[222:225], v[12:15]
	v_mfma_f32_16x16x32_bf16 v[4:7], v[100:103], v[222:225], v[4:7]
	v_mfma_f32_16x16x32_bf16 v[56:59], v[162:165], v[194:197], v[56:59]
	v_mfma_f32_16x16x32_bf16 v[48:51], v[186:189], v[194:197], v[48:51]
	v_mfma_f32_16x16x32_bf16 v[40:43], v[162:165], v[202:205], v[40:43]
	v_mfma_f32_16x16x32_bf16 v[32:35], v[186:189], v[202:205], v[32:35]
	v_mfma_f32_16x16x32_bf16 v[24:27], v[162:165], v[210:213], v[24:27]
	v_mfma_f32_16x16x32_bf16 v[16:19], v[186:189], v[210:213], v[16:19]
	v_mfma_f32_16x16x32_bf16 v[8:11], v[162:165], v[218:221], v[8:11]
	v_mfma_f32_16x16x32_bf16 v[0:3], v[186:189], v[218:221], v[0:3]
	v_mfma_f32_16x16x32_bf16 v[56:59], v[182:185], v[198:201], v[56:59]
	v_mfma_f32_16x16x32_bf16 v[48:51], v[190:193], v[198:201], v[48:51]
	v_mfma_f32_16x16x32_bf16 v[40:43], v[182:185], v[206:209], v[40:43]
	v_mfma_f32_16x16x32_bf16 v[32:35], v[190:193], v[206:209], v[32:35]
	v_mfma_f32_16x16x32_bf16 v[24:27], v[182:185], v[214:217], v[24:27]
	v_mfma_f32_16x16x32_bf16 v[16:19], v[190:193], v[214:217], v[16:19]
	v_mfma_f32_16x16x32_bf16 v[8:11], v[182:185], v[222:225], v[8:11]
	v_mfma_f32_16x16x32_bf16 v[0:3], v[190:193], v[222:225], v[0:3]
	s_barrier
	s_add_i32 s63, 0, 0x18000
	s_add_i32 s64, 0, 0x1c000
	ds_read_b128 v[80:83], v166 offset:32768
	ds_read_b128 v[84:87], v166 offset:33792
	ds_read_b128 v[96:99], v166 offset:34816
	ds_read_b128 v[100:103], v166 offset:35840
	ds_read_b128 v[162:165], v166 offset:49152
	ds_read_b128 v[182:185], v166 offset:50176
	ds_read_b128 v[186:189], v166 offset:51200
	ds_read_b128 v[190:193], v166 offset:52224
	s_add_u32 s22, s22, 0x4000
	s_addc_u32 s23, s23, 0
	s_mov_b32 m0, s47
	ds_read_b128 v[194:197], v180 offset:32768
	ds_read_b128 v[198:201], v180 offset:33792
	ds_read_b128 v[202:205], v180 offset:34816
	ds_read_b128 v[206:209], v180 offset:35840
	ds_read_b128 v[210:213], v180 offset:36864
	ds_read_b128 v[214:217], v180 offset:37888
	ds_read_b128 v[218:221], v180 offset:38912
	ds_read_b128 v[222:225], v180 offset:39936
	global_load_lds_dwordx4 v152, s[22:23]
	s_mov_b32 m0, s48
	s_nop 0
	global_load_lds_dwordx4 v148, s[22:23]
	s_waitcnt vmcnt(8)
	s_waitcnt lgkmcnt(0)
	s_barrier
; #define PG8_STAGE(bufoff, gbase, voff) do { _Pragma("unroll") for (int _i = 0; _i < 2; ++_i) \
;         __builtin_amdgcn_global_load_lds((const unsigned*)((const char*)(gbase) + (voff)[_i]), (PG8_LAS unsigned*)(lds + (bufoff) + ldsw + _i * 8192), 16, 0, 0); } while (0)
; #define PG8_LDA(dst, b, h) do { _Pragma("unroll") for (int m = 0; m < 4; ++m) _Pragma("unroll") for (int k = 0; k < 2; ++k) dst[m][k] = *(const PG8_LAS bf16x8*)(lds + PG8_SA(b, h) + aoff + m * 2048 + k * 1024); } while (0)
; #define PG8_MMA(ai, bj, At, Bt) do { __builtin_amdgcn_s_setprio(1); _Pragma("unroll") for (int m = 0; m < 4; ++m) _Pragma("unroll") for (int n = 0; n < 2; ++n) _Pragma("unroll") for (int k = 0; k < 2; ++k) \
;         acc[ai][bj][m][n] = __builtin_amdgcn_mfma_f32_16x16x32_bf16(Bt[n][k], At[m][k], acc[ai][bj][m][n], 0, 0, 0); __builtin_amdgcn_s_setprio(0); } while (0)
; #define PG8_WAIT_V(n) asm volatile("s_waitcnt vmcnt(" #n ")" ::: "memory")
; #define PG8_WAIT_L(n) asm volatile("s_waitcnt lgkmcnt(" #n ")" ::: "memory")
; #define PG8_BAR __builtin_amdgcn_s_barrier()
; #define PG8_SCHED __builtin_amdgcn_sched_barrier(0)
; template <class Epi, class Sched, bool ALIGN_EPI>
; __device__ __forceinline__ void gemm_phase(PG8_LAS unsigned char* lds, const Gemm g, const Sched& S, const Epi& E, const int tid) {
;     ...
;             PG8_WAIT_V(8); PG8_WAIT_L(0); PG8_BAR; PG8_MMA(0, 0, At, B0); PG8_MMA(0, 1, At, B1); PG8_BAR; PG8_SCHED;
;             PG8_LDA(At, 1, 1); PG8_STAGE(PG8_SB(1, 0), b3, voffB); PG8_STAGE(PG8_SB(1, 1), b3 + hstepB, voffB); PG8_STAGE(PG8_SA(1, 0), a3, voffA);
;             PG8_WAIT_V(8); PG8_WAIT_L(0); PG8_BAR; PG8_MMA(1, 0, At, B0); PG8_MMA(1, 1, At, B1); PG8_BAR; PG8_SCHED;
;         }
;         if constexpr (ALIGN_EPI) { if (wr == 0) PG8_BAR; }
	v_mfma_f32_16x16x32_bf16 v[142:145], v[80:83], v[194:197], v[142:145]
	v_mfma_f32_16x16x32_bf16 v[134:137], v[96:99], v[194:197], v[134:137]
	v_mfma_f32_16x16x32_bf16 v[124:127], v[80:83], v[202:205], v[124:127]
	v_mfma_f32_16x16x32_bf16 v[116:119], v[96:99], v[202:205], v[116:119]
	v_mfma_f32_16x16x32_bf16 v[108:111], v[80:83], v[210:213], v[108:111]
	v_mfma_f32_16x16x32_bf16 v[92:95], v[96:99], v[210:213], v[92:95]
	v_mfma_f32_16x16x32_bf16 v[76:79], v[80:83], v[218:221], v[76:79]
	v_mfma_f32_16x16x32_bf16 v[68:71], v[96:99], v[218:221], v[68:71]
	v_mfma_f32_16x16x32_bf16 v[142:145], v[84:87], v[198:201], v[142:145]
	v_mfma_f32_16x16x32_bf16 v[134:137], v[100:103], v[198:201], v[134:137]
	v_mfma_f32_16x16x32_bf16 v[124:127], v[84:87], v[206:209], v[124:127]
	v_mfma_f32_16x16x32_bf16 v[116:119], v[100:103], v[206:209], v[116:119]
	v_mfma_f32_16x16x32_bf16 v[108:111], v[84:87], v[214:217], v[108:111]
	v_mfma_f32_16x16x32_bf16 v[92:95], v[100:103], v[214:217], v[92:95]
	v_mfma_f32_16x16x32_bf16 v[76:79], v[84:87], v[222:225], v[76:79]
	v_mfma_f32_16x16x32_bf16 v[68:71], v[100:103], v[222:225], v[68:71]
	v_mfma_f32_16x16x32_bf16 v[138:141], v[162:165], v[194:197], v[138:141]
	v_mfma_f32_16x16x32_bf16 v[130:133], v[186:189], v[194:197], v[130:133]
	v_mfma_f32_16x16x32_bf16 v[120:123], v[162:165], v[202:205], v[120:123]
	v_mfma_f32_16x16x32_bf16 v[112:115], v[186:189], v[202:205], v[112:115]
	v_mfma_f32_16x16x32_bf16 v[104:107], v[162:165], v[210:213], v[104:107]
	v_mfma_f32_16x16x32_bf16 v[88:91], v[186:189], v[210:213], v[88:91]
	v_mfma_f32_16x16x32_bf16 v[72:75], v[162:165], v[218:221], v[72:75]
	v_mfma_f32_16x16x32_bf16 v[64:67], v[186:189], v[218:221], v[64:67]
	v_mfma_f32_16x16x32_bf16 v[138:141], v[182:185], v[198:201], v[138:141]
	v_mfma_f32_16x16x32_bf16 v[130:133], v[190:193], v[198:201], v[130:133]
	v_mfma_f32_16x16x32_bf16 v[120:123], v[182:185], v[206:209], v[120:123]
	v_mfma_f32_16x16x32_bf16 v[112:115], v[190:193], v[206:209], v[112:115]
	v_mfma_f32_16x16x32_bf16 v[104:107], v[182:185], v[214:217], v[104:107]
	v_mfma_f32_16x16x32_bf16 v[88:91], v[190:193], v[214:217], v[88:91]
	v_mfma_f32_16x16x32_bf16 v[72:75], v[182:185], v[222:225], v[72:75]
	v_mfma_f32_16x16x32_bf16 v[64:67], v[190:193], v[222:225], v[64:67]
	s_barrier
	s_add_u32 s22, s20, 0x8000
	s_addc_u32 s23, s21, 0
	s_add_i32 s63, s63, s42
	s_mov_b32 m0, s63
	ds_read_b128 v[194:197], v180 offset:49152
	ds_read_b128 v[198:201], v180 offset:50176
	ds_read_b128 v[202:205], v180 offset:51200
	ds_read_b128 v[206:209], v180 offset:52224
	ds_read_b128 v[210:213], v180 offset:53248
	ds_read_b128 v[214:217], v180 offset:54272
	ds_read_b128 v[218:221], v180 offset:55296
	ds_read_b128 v[222:225], v180 offset:56320
	global_load_lds_dwordx4 v150, s[22:23]
	s_add_i32 m0, s63, 0x2000
	s_add_u32 s20, s20, 0xc000
	s_addc_u32 s21, s21, 0
	global_load_lds_dwordx4 v146, s[22:23]
	s_add_i32 s22, s64, s42
	s_mov_b32 m0, s22
	s_nop 0
	global_load_lds_dwordx4 v150, s[20:21]
	s_add_i32 m0, s22, 0x2000
	s_nop 0
	global_load_lds_dwordx4 v146, s[20:21]
	s_mov_b32 m0, s51
	s_nop 0
	global_load_lds_dwordx4 v152, s[18:19]
	s_mov_b32 m0, s52
	s_nop 0
	global_load_lds_dwordx4 v148, s[18:19]
	s_waitcnt vmcnt(8)
	s_waitcnt lgkmcnt(0)
	s_barrier
	v_mfma_f32_16x16x32_bf16 v[60:63], v[80:83], v[194:197], v[60:63]
	v_mfma_f32_16x16x32_bf16 v[52:55], v[96:99], v[194:197], v[52:55]
	v_mfma_f32_16x16x32_bf16 v[44:47], v[80:83], v[202:205], v[44:47]
	v_mfma_f32_16x16x32_bf16 v[36:39], v[96:99], v[202:205], v[36:39]
	v_mfma_f32_16x16x32_bf16 v[28:31], v[80:83], v[210:213], v[28:31]
	v_mfma_f32_16x16x32_bf16 v[20:23], v[96:99], v[210:213], v[20:23]
	v_mfma_f32_16x16x32_bf16 v[12:15], v[80:83], v[218:221], v[12:15]
	v_mfma_f32_16x16x32_bf16 v[4:7], v[96:99], v[218:221], v[4:7]
	v_mfma_f32_16x16x32_bf16 v[60:63], v[84:87], v[198:201], v[60:63]
	v_mfma_f32_16x16x32_bf16 v[52:55], v[100:103], v[198:201], v[52:55]
	v_mfma_f32_16x16x32_bf16 v[44:47], v[84:87], v[206:209], v[44:47]
	v_mfma_f32_16x16x32_bf16 v[36:39], v[100:103], v[206:209], v[36:39]
	v_mfma_f32_16x16x32_bf16 v[28:31], v[84:87], v[214:217], v[28:31]
	v_mfma_f32_16x16x32_bf16 v[20:23], v[100:103], v[214:217], v[20:23]
	v_mfma_f32_16x16x32_bf16 v[12:15], v[84:87], v[222:225], v[12:15]
	v_mfma_f32_16x16x32_bf16 v[4:7], v[100:103], v[222:225], v[4:7]
	v_mfma_f32_16x16x32_bf16 v[56:59], v[162:165], v[194:197], v[56:59]
	v_mfma_f32_16x16x32_bf16 v[48:51], v[186:189], v[194:197], v[48:51]
	v_mfma_f32_16x16x32_bf16 v[40:43], v[162:165], v[202:205], v[40:43]
	v_mfma_f32_16x16x32_bf16 v[32:35], v[186:189], v[202:205], v[32:35]
	v_mfma_f32_16x16x32_bf16 v[24:27], v[162:165], v[210:213], v[24:27]
	v_mfma_f32_16x16x32_bf16 v[16:19], v[186:189], v[210:213], v[16:19]
	v_mfma_f32_16x16x32_bf16 v[8:11], v[162:165], v[218:221], v[8:11]
	v_mfma_f32_16x16x32_bf16 v[0:3], v[186:189], v[218:221], v[0:3]
	v_mfma_f32_16x16x32_bf16 v[56:59], v[182:185], v[198:201], v[56:59]
	v_mfma_f32_16x16x32_bf16 v[48:51], v[190:193], v[198:201], v[48:51]
	v_mfma_f32_16x16x32_bf16 v[40:43], v[182:185], v[206:209], v[40:43]
	v_mfma_f32_16x16x32_bf16 v[32:35], v[190:193], v[206:209], v[32:35]
	v_mfma_f32_16x16x32_bf16 v[24:27], v[182:185], v[214:217], v[24:27]
	v_mfma_f32_16x16x32_bf16 v[16:19], v[190:193], v[214:217], v[16:19]
	v_mfma_f32_16x16x32_bf16 v[8:11], v[182:185], v[222:225], v[8:11]
	v_mfma_f32_16x16x32_bf16 v[0:3], v[190:193], v[222:225], v[0:3]
	s_barrier
	s_add_i32 s62, s62, 2
	s_add_u32 s16, s16, 0x10000
	s_addc_u32 s17, s17, 0
	s_add_u32 s60, s60, 0x10000
	s_addc_u32 s61, s61, 0
	s_cmp_gt_u32 s62, 29
	s_cbranch_scc0 .LBB0_246
	s_and_b64 vcc, exec, s[6:7]
	s_cbranch_vccz .LBB0_249
	s_barrier

; #define PG8_WAIT_V(n) asm volatile("s_waitcnt vmcnt(" #n ")" ::: "memory")
; #define PG8_BAR __builtin_amdgcn_s_barrier()
; template <class Epi, class Sched, bool ALIGN_EPI>
; __device__ __forceinline__ void gemm_phase(PG8_LAS unsigned char* lds, const Gemm g, const Sched& S, const Epi& E, const int tid) {
;     ...
;     PG8_WAIT_V(0);
;     if constexpr (!ALIGN_EPI) { if (wr == 0) PG8_BAR; }
;     PG8_BAR;
.LBB0_252:
	s_setprio 0
	s_waitcnt vmcnt(0)
	s_barrier

; #define PG8_STAGE(bufoff, gbase, voff) do { _Pragma("unroll") for (int _i = 0; _i < 2; ++_i) \
;         __builtin_amdgcn_global_load_lds((const unsigned*)((const char*)(gbase) + (voff)[_i]), (PG8_LAS unsigned*)(lds + (bufoff) + ldsw + _i * 8192), 16, 0, 0); } while (0)
; #define PG8_LDA(dst, b, h) do { _Pragma("unroll") for (int m = 0; m < 4; ++m) _Pragma("unroll") for (int k = 0; k < 2; ++k) dst[m][k] = *(const PG8_LAS bf16x8*)(lds + PG8_SA(b, h) + aoff + m * 2048 + k * 1024); } while (0)
; #define PG8_LDB(dst, b, h) do { _Pragma("unroll") for (int n = 0; n < 2; ++n) _Pragma("unroll") for (int k = 0; k < 2; ++k) dst[n][k] = *(const PG8_LAS bf16x8*)(lds + PG8_SB(b, h) + boff + n * 2048 + k * 1024); } while (0)
; #define PG8_MMA(ai, bj, At, Bt) do { __builtin_amdgcn_s_setprio(1); _Pragma("unroll") for (int m = 0; m < 4; ++m) _Pragma("unroll") for (int n = 0; n < 2; ++n) _Pragma("unroll") for (int k = 0; k < 2; ++k) \
;         acc[ai][bj][m][n] = __builtin_amdgcn_mfma_f32_16x16x32_bf16(Bt[n][k], At[m][k], acc[ai][bj][m][n], 0, 0, 0); __builtin_amdgcn_s_setprio(0); } while (0)
; #define PG8_BAR __builtin_amdgcn_s_barrier()
; template <class Epi, class Sched, bool ALIGN_EPI>
; __device__ __forceinline__ void gemm_phase(PG8_LAS unsigned char* lds, const Gemm g, const Sched& S, const Epi& E, const int tid) {
;     ...
;         const bool has_next = S.next(ui + 1, nxt);
;         const char* nA = has_next ? (const char*)g.A + (size_t)nxt.pm * tstepA + PG8_ACOL(nxt) : cA; const char* nB = has_next ? (const char*)g.Bt + (size_t)nxt.pn * tstepB : cB;
;         for (int t = 0; t < nt; t += 2) {
;             const bool last = (t == nt - 2);
;             const char* a1 = cA + (size_t)(t + 1) * kstepA;
;             const char* a2 = last ? nA : cA + (size_t)(t + 2) * kstepA; const char* b2 = last ? nB : cB + (size_t)(t + 2) * kstepB;
;             const char* a3 = a2 + kstepA; const char* b3 = b2 + kstepB;
;             if (last && has_next) S.a_ready(nxt);
;             PG8_LDB(B0, 0, 0); PG8_LDB(B1, 0, 1); PG8_SCHED; PG8_LDA(At, 0, 0); PG8_STAGE(PG8_SA(1, 1), a1 + hstepA, voffA);
;             PG8_WAIT_V(8); PG8_WAIT_L(0); PG8_BAR; PG8_MMA(0, 0, At, B0); PG8_MMA(0, 1, At, B1); PG8_BAR; PG8_SCHED;
;             PG8_LDA(At, 0, 1); PG8_STAGE(PG8_SB(0, 0), b2, voffB); PG8_STAGE(PG8_SB(0, 1), b2 + hstepB, voffB); PG8_STAGE(PG8_SA(0, 0), a2, voffA);
.LBB0_341:
	s_ashr_i32 s47, s46, 31
	s_lshl_b64 s[48:49], s[46:47], 20
	s_add_u32 s48, s57, s48
	s_addc_u32 s49, s58, s49
	s_and_b64 s[50:51], s[6:7], exec
	s_cselect_b32 s9, s49, s11
	s_cselect_b32 s43, s48, s10
	s_ashr_i32 s45, s44, 31
	s_lshl_b64 s[50:51], s[44:45], 20
	s_add_u32 s50, s56, s50
	s_addc_u32 s51, s33, s51
	s_and_b64 s[52:53], s[6:7], exec
	s_cselect_b32 s45, s51, s13
	s_cselect_b32 s47, s50, s12
	s_add_u32 s10, s10, 0xc000
	s_addc_u32 s11, s11, 0
	s_add_u32 s79, s12, 0x10000
	s_addc_u32 s80, s13, 0
	s_mov_b32 s81, -2
	s_waitcnt lgkmcnt(0)
	s_waitcnt vmcnt(0)
	v_add_u32_e32 v166, 0x10000, v171
	s_add_u32 s12, s10, 0x4000
	s_addc_u32 s13, s11, 0
	s_cmp_eq_u32 s81, 28
	s_cselect_b32 s54, s43, s12
	s_cselect_b32 s55, s9, s13
	s_cselect_b32 s52, s47, s79
	s_cselect_b32 s53, s45, s80
	s_add_u32 s12, s54, 0x8000
	s_addc_u32 s13, s55, 0
	s_add_i32 s82, 0, 0x10000
	s_add_i32 s84, 0, 0x14000
	ds_read_b128 v[48:51], v166
	ds_read_b128 v[52:55], v166 offset:1024
	ds_read_b128 v[64:67], v166 offset:2048
	ds_read_b128 v[68:71], v166 offset:3072
	ds_read_b128 v[146:149], v166 offset:16384
	ds_read_b128 v[150:153], v166 offset:17408
	ds_read_b128 v[180:183], v166 offset:18432
	ds_read_b128 v[184:187], v166 offset:19456
	s_add_i32 m0, s62, 0xc000
	ds_read_b128 v[188:191], v210
	ds_read_b128 v[192:195], v210 offset:1024
	ds_read_b128 v[196:199], v210 offset:2048
	ds_read_b128 v[200:203], v210 offset:3072
	ds_read_b128 v[204:207], v210 offset:4096
	ds_read_b128 v[212:215], v210 offset:5120
	ds_read_b128 v[216:219], v210 offset:6144
	ds_read_b128 v[220:223], v210 offset:7168
	global_load_lds_dwordx4 v176, s[10:11]
	s_add_i32 m0, s62, 0xe000
	s_nop 0
	global_load_lds_dwordx4 v178, s[10:11]
	s_waitcnt vmcnt(8)
	s_waitcnt lgkmcnt(0)
	s_and_b64 vcc, exec, s[34:35]
	s_cbranch_vccnz .Lsprio_1
	s_setprio 1
.Lsprio_1:
	s_barrier
	v_mfma_f32_16x16x32_bf16 v[142:145], v[48:51], v[188:191], 0
	v_mfma_f32_16x16x32_bf16 v[138:141], v[64:67], v[188:191], 0
	v_mfma_f32_16x16x32_bf16 v[124:127], v[48:51], v[196:199], 0
	v_mfma_f32_16x16x32_bf16 v[120:123], v[64:67], v[196:199], 0
	v_mfma_f32_16x16x32_bf16 v[108:111], v[48:51], v[204:207], 0
	v_mfma_f32_16x16x32_bf16 v[104:107], v[64:67], v[204:207], 0
	v_mfma_f32_16x16x32_bf16 v[92:95], v[48:51], v[216:219], 0
	v_mfma_f32_16x16x32_bf16 v[88:91], v[64:67], v[216:219], 0
	v_mfma_f32_16x16x32_bf16 v[142:145], v[52:55], v[192:195], v[142:145]
	v_mfma_f32_16x16x32_bf16 v[138:141], v[68:71], v[192:195], v[138:141]
	v_mfma_f32_16x16x32_bf16 v[124:127], v[52:55], v[200:203], v[124:127]
	v_mfma_f32_16x16x32_bf16 v[120:123], v[68:71], v[200:203], v[120:123]
	v_mfma_f32_16x16x32_bf16 v[108:111], v[52:55], v[212:215], v[108:111]
	v_mfma_f32_16x16x32_bf16 v[104:107], v[68:71], v[212:215], v[104:107]
	v_mfma_f32_16x16x32_bf16 v[92:95], v[52:55], v[220:223], v[92:95]
	v_mfma_f32_16x16x32_bf16 v[88:91], v[68:71], v[220:223], v[88:91]
	v_mfma_f32_16x16x32_bf16 v[134:137], v[146:149], v[188:191], 0
	v_mfma_f32_16x16x32_bf16 v[130:133], v[180:183], v[188:191], 0
	v_mfma_f32_16x16x32_bf16 v[116:119], v[146:149], v[196:199], 0
	v_mfma_f32_16x16x32_bf16 v[112:115], v[180:183], v[196:199], 0
	v_mfma_f32_16x16x32_bf16 v[100:103], v[146:149], v[204:207], 0
	v_mfma_f32_16x16x32_bf16 v[96:99], v[180:183], v[204:207], 0
	v_mfma_f32_16x16x32_bf16 v[84:87], v[146:149], v[216:219], 0
	v_mfma_f32_16x16x32_bf16 v[80:83], v[180:183], v[216:219], 0
	v_mfma_f32_16x16x32_bf16 v[134:137], v[150:153], v[192:195], v[134:137]
	v_mfma_f32_16x16x32_bf16 v[130:133], v[184:187], v[192:195], v[130:133]
	v_mfma_f32_16x16x32_bf16 v[116:119], v[150:153], v[200:203], v[116:119]
	v_mfma_f32_16x16x32_bf16 v[112:115], v[184:187], v[200:203], v[112:115]
	v_mfma_f32_16x16x32_bf16 v[100:103], v[150:153], v[212:215], v[100:103]
	v_mfma_f32_16x16x32_bf16 v[96:99], v[184:187], v[212:215], v[96:99]
	v_mfma_f32_16x16x32_bf16 v[84:87], v[150:153], v[220:223], v[84:87]
	v_mfma_f32_16x16x32_bf16 v[80:83], v[184:187], v[220:223], v[80:83]
	s_barrier
	s_add_i32 s82, s82, s59
	s_mov_b32 m0, s82
	ds_read_b128 v[188:191], v210 offset:16384
	ds_read_b128 v[192:195], v210 offset:17408
	ds_read_b128 v[196:199], v210 offset:18432
	ds_read_b128 v[200:203], v210 offset:19456
	ds_read_b128 v[204:207], v210 offset:20480
	ds_read_b128 v[212:215], v210 offset:21504
	ds_read_b128 v[216:219], v210 offset:22528
	ds_read_b128 v[220:223], v210 offset:23552
	global_load_lds_dwordx4 v156, s[52:53]
	s_add_i32 m0, s82, 0x2000
	s_add_u32 s82, s52, 0x4000
	s_addc_u32 s83, s53, 0
	s_add_i32 s84, s84, s59
	global_load_lds_dwordx4 v160, s[52:53]
	s_mov_b32 m0, s84
	s_nop 0
	global_load_lds_dwordx4 v156, s[82:83]
	s_add_i32 m0, s84, 0x2000
	s_nop 0
	global_load_lds_dwordx4 v160, s[82:83]
	s_mov_b32 m0, s62
	s_nop 0
	global_load_lds_dwordx4 v154, s[54:55]
	s_mov_b32 m0, s63
	s_nop 0
	global_load_lds_dwordx4 v158, s[54:55]
	s_waitcnt vmcnt(8)
	s_waitcnt lgkmcnt(0)
	s_barrier
; #define PG8_STAGE(bufoff, gbase, voff) do { _Pragma("unroll") for (int _i = 0; _i < 2; ++_i) \
;         __builtin_amdgcn_global_load_lds((const unsigned*)((const char*)(gbase) + (voff)[_i]), (PG8_LAS unsigned*)(lds + (bufoff) + ldsw + _i * 8192), 16, 0, 0); } while (0)
; #define PG8_LDA(dst, b, h) do { _Pragma("unroll") for (int m = 0; m < 4; ++m) _Pragma("unroll") for (int k = 0; k < 2; ++k) dst[m][k] = *(const PG8_LAS bf16x8*)(lds + PG8_SA(b, h) + aoff + m * 2048 + k * 1024); } while (0)
; #define PG8_LDB(dst, b, h) do { _Pragma("unroll") for (int n = 0; n < 2; ++n) _Pragma("unroll") for (int k = 0; k < 2; ++k) dst[n][k] = *(const PG8_LAS bf16x8*)(lds + PG8_SB(b, h) + boff + n * 2048 + k * 1024); } while (0)
; #define PG8_MMA(ai, bj, At, Bt) do { __builtin_amdgcn_s_setprio(1); _Pragma("unroll") for (int m = 0; m < 4; ++m) _Pragma("unroll") for (int n = 0; n < 2; ++n) _Pragma("unroll") for (int k = 0; k < 2; ++k) \
;         acc[ai][bj][m][n] = __builtin_amdgcn_mfma_f32_16x16x32_bf16(Bt[n][k], At[m][k], acc[ai][bj][m][n], 0, 0, 0); __builtin_amdgcn_s_setprio(0); } while (0)
; #define PG8_WAIT_V(n) asm volatile("s_waitcnt vmcnt(" #n ")" ::: "memory")
; #define PG8_WAIT_L(n) asm volatile("s_waitcnt lgkmcnt(" #n ")" ::: "memory")
; #define PG8_BAR __builtin_amdgcn_s_barrier()
; #define PG8_SCHED __builtin_amdgcn_sched_barrier(0)
; template <class Epi, class Sched, bool ALIGN_EPI>
; __device__ __forceinline__ void gemm_phase(PG8_LAS unsigned char* lds, const Gemm g, const Sched& S, const Epi& E, const int tid) {
;     ...
;             PG8_WAIT_V(8); PG8_WAIT_L(0); PG8_BAR; PG8_MMA(1, 0, At, B0); PG8_MMA(1, 1, At, B1); PG8_BAR; PG8_SCHED;
;             PG8_LDB(B0, 1, 0); PG8_LDB(B1, 1, 1); PG8_SCHED; PG8_LDA(At, 1, 0); PG8_STAGE(PG8_SA(0, 1), a2 + hstepA, voffA);
;             PG8_WAIT_V(8); PG8_WAIT_L(0); PG8_BAR; PG8_MMA(0, 0, At, B0); PG8_MMA(0, 1, At, B1); PG8_BAR; PG8_SCHED;
;             PG8_LDA(At, 1, 1); PG8_STAGE(PG8_SB(1, 0), b3, voffB); PG8_STAGE(PG8_SB(1, 1), b3 + hstepB, voffB); PG8_STAGE(PG8_SA(1, 0), a3, voffA);
	v_mfma_f32_16x16x32_bf16 v[76:79], v[48:51], v[188:191], 0
	v_mfma_f32_16x16x32_bf16 v[72:75], v[64:67], v[188:191], 0
	v_mfma_f32_16x16x32_bf16 v[44:47], v[48:51], v[196:199], 0
	v_mfma_f32_16x16x32_bf16 v[40:43], v[64:67], v[196:199], 0
	v_mfma_f32_16x16x32_bf16 v[28:31], v[48:51], v[204:207], 0
	v_mfma_f32_16x16x32_bf16 v[24:27], v[64:67], v[204:207], 0
	v_mfma_f32_16x16x32_bf16 v[12:15], v[48:51], v[216:219], 0
	v_mfma_f32_16x16x32_bf16 v[8:11], v[64:67], v[216:219], 0
	v_mfma_f32_16x16x32_bf16 v[76:79], v[52:55], v[192:195], v[76:79]
	v_mfma_f32_16x16x32_bf16 v[72:75], v[68:71], v[192:195], v[72:75]
	v_mfma_f32_16x16x32_bf16 v[44:47], v[52:55], v[200:203], v[44:47]
	v_mfma_f32_16x16x32_bf16 v[40:43], v[68:71], v[200:203], v[40:43]
	v_mfma_f32_16x16x32_bf16 v[28:31], v[52:55], v[212:215], v[28:31]
	v_mfma_f32_16x16x32_bf16 v[24:27], v[68:71], v[212:215], v[24:27]
	v_mfma_f32_16x16x32_bf16 v[12:15], v[52:55], v[220:223], v[12:15]
	v_mfma_f32_16x16x32_bf16 v[8:11], v[68:71], v[220:223], v[8:11]
	v_mfma_f32_16x16x32_bf16 v[36:39], v[146:149], v[196:199], 0
	v_mfma_f32_16x16x32_bf16 v[32:35], v[180:183], v[196:199], 0
	v_mfma_f32_16x16x32_bf16 v[20:23], v[146:149], v[204:207], 0
	v_mfma_f32_16x16x32_bf16 v[16:19], v[180:183], v[204:207], 0
	v_mfma_f32_16x16x32_bf16 v[4:7], v[146:149], v[216:219], 0
	v_mfma_f32_16x16x32_bf16 v[0:3], v[180:183], v[216:219], 0
	v_mfma_f32_16x16x32_bf16 v[48:51], v[146:149], v[188:191], 0
	v_mfma_f32_16x16x32_bf16 v[52:55], v[180:183], v[188:191], 0
	v_mfma_f32_16x16x32_bf16 v[36:39], v[150:153], v[200:203], v[36:39]
	v_mfma_f32_16x16x32_bf16 v[32:35], v[184:187], v[200:203], v[32:35]
	v_mfma_f32_16x16x32_bf16 v[20:23], v[150:153], v[212:215], v[20:23]
	v_mfma_f32_16x16x32_bf16 v[16:19], v[184:187], v[212:215], v[16:19]
	v_mfma_f32_16x16x32_bf16 v[4:7], v[150:153], v[220:223], v[4:7]
	v_mfma_f32_16x16x32_bf16 v[0:3], v[184:187], v[220:223], v[0:3]
	v_mfma_f32_16x16x32_bf16 v[48:51], v[150:153], v[192:195], v[48:51]
	v_mfma_f32_16x16x32_bf16 v[52:55], v[184:187], v[192:195], v[52:55]
	s_barrier
	s_add_i32 s82, 0, 0x18000
	s_add_i32 s83, 0, 0x1c000
	ds_read_b128 v[56:59], v166 offset:32768
	ds_read_b128 v[60:63], v166 offset:33792
	ds_read_b128 v[64:67], v166 offset:34816
	ds_read_b128 v[68:71], v166 offset:35840
	ds_read_b128 v[146:149], v166 offset:49152
	ds_read_b128 v[150:153], v166 offset:50176
	ds_read_b128 v[180:183], v166 offset:51200
	ds_read_b128 v[184:187], v166 offset:52224
	s_add_u32 s54, s54, 0x4000
	s_addc_u32 s55, s55, 0
	s_mov_b32 m0, s64
	ds_read_b128 v[188:191], v210 offset:32768
	ds_read_b128 v[192:195], v210 offset:33792
	ds_read_b128 v[196:199], v210 offset:34816
	ds_read_b128 v[200:203], v210 offset:35840
	ds_read_b128 v[204:207], v210 offset:36864
	ds_read_b128 v[212:215], v210 offset:37888
	ds_read_b128 v[216:219], v210 offset:38912
	ds_read_b128 v[220:223], v210 offset:39936
	global_load_lds_dwordx4 v154, s[54:55]
	s_mov_b32 m0, s65
	s_nop 0
	global_load_lds_dwordx4 v158, s[54:55]
	s_waitcnt vmcnt(8)
	s_waitcnt lgkmcnt(0)
	s_barrier
	v_mfma_f32_16x16x32_bf16 v[142:145], v[56:59], v[188:191], v[142:145]
	v_mfma_f32_16x16x32_bf16 v[138:141], v[64:67], v[188:191], v[138:141]
	v_mfma_f32_16x16x32_bf16 v[124:127], v[56:59], v[196:199], v[124:127]
	v_mfma_f32_16x16x32_bf16 v[120:123], v[64:67], v[196:199], v[120:123]
	v_mfma_f32_16x16x32_bf16 v[108:111], v[56:59], v[204:207], v[108:111]
	v_mfma_f32_16x16x32_bf16 v[104:107], v[64:67], v[204:207], v[104:107]
	v_mfma_f32_16x16x32_bf16 v[92:95], v[56:59], v[216:219], v[92:95]
	v_mfma_f32_16x16x32_bf16 v[88:91], v[64:67], v[216:219], v[88:91]
	v_mfma_f32_16x16x32_bf16 v[142:145], v[60:63], v[192:195], v[142:145]
	v_mfma_f32_16x16x32_bf16 v[138:141], v[68:71], v[192:195], v[138:141]
	v_mfma_f32_16x16x32_bf16 v[124:127], v[60:63], v[200:203], v[124:127]
	v_mfma_f32_16x16x32_bf16 v[120:123], v[68:71], v[200:203], v[120:123]
	v_mfma_f32_16x16x32_bf16 v[108:111], v[60:63], v[212:215], v[108:111]
	v_mfma_f32_16x16x32_bf16 v[104:107], v[68:71], v[212:215], v[104:107]
	v_mfma_f32_16x16x32_bf16 v[92:95], v[60:63], v[220:223], v[92:95]
	v_mfma_f32_16x16x32_bf16 v[88:91], v[68:71], v[220:223], v[88:91]
	v_mfma_f32_16x16x32_bf16 v[134:137], v[146:149], v[188:191], v[134:137]
	v_mfma_f32_16x16x32_bf16 v[130:133], v[180:183], v[188:191], v[130:133]
	v_mfma_f32_16x16x32_bf16 v[116:119], v[146:149], v[196:199], v[116:119]
	v_mfma_f32_16x16x32_bf16 v[112:115], v[180:183], v[196:199], v[112:115]
	v_mfma_f32_16x16x32_bf16 v[100:103], v[146:149], v[204:207], v[100:103]
	v_mfma_f32_16x16x32_bf16 v[96:99], v[180:183], v[204:207], v[96:99]
	v_mfma_f32_16x16x32_bf16 v[84:87], v[146:149], v[216:219], v[84:87]
	v_mfma_f32_16x16x32_bf16 v[80:83], v[180:183], v[216:219], v[80:83]
	v_mfma_f32_16x16x32_bf16 v[134:137], v[150:153], v[192:195], v[134:137]
	v_mfma_f32_16x16x32_bf16 v[130:133], v[184:187], v[192:195], v[130:133]
	v_mfma_f32_16x16x32_bf16 v[116:119], v[150:153], v[200:203], v[116:119]
	v_mfma_f32_16x16x32_bf16 v[112:115], v[184:187], v[200:203], v[112:115]
	v_mfma_f32_16x16x32_bf16 v[100:103], v[150:153], v[212:215], v[100:103]
	v_mfma_f32_16x16x32_bf16 v[96:99], v[184:187], v[212:215], v[96:99]
	v_mfma_f32_16x16x32_bf16 v[84:87], v[150:153], v[220:223], v[84:87]
	v_mfma_f32_16x16x32_bf16 v[80:83], v[184:187], v[220:223], v[80:83]
	s_barrier
; #define PG8_STAGE(bufoff, gbase, voff) do { _Pragma("unroll") for (int _i = 0; _i < 2; ++_i) \
;         __builtin_amdgcn_global_load_lds((const unsigned*)((const char*)(gbase) + (voff)[_i]), (PG8_LAS unsigned*)(lds + (bufoff) + ldsw + _i * 8192), 16, 0, 0); } while (0)
; #define PG8_LDA(dst, b, h) do { _Pragma("unroll") for (int m = 0; m < 4; ++m) _Pragma("unroll") for (int k = 0; k < 2; ++k) dst[m][k] = *(const PG8_LAS bf16x8*)(lds + PG8_SA(b, h) + aoff + m * 2048 + k * 1024); } while (0)
; #define PG8_LDB(dst, b, h) do { _Pragma("unroll") for (int n = 0; n < 2; ++n) _Pragma("unroll") for (int k = 0; k < 2; ++k) dst[n][k] = *(const PG8_LAS bf16x8*)(lds + PG8_SB(b, h) + boff + n * 2048 + k * 1024); } while (0)
; #define PG8_MMA(ai, bj, At, Bt) do { __builtin_amdgcn_s_setprio(1); _Pragma("unroll") for (int m = 0; m < 4; ++m) _Pragma("unroll") for (int n = 0; n < 2; ++n) _Pragma("unroll") for (int k = 0; k < 2; ++k) \
;         acc[ai][bj][m][n] = __builtin_amdgcn_mfma_f32_16x16x32_bf16(Bt[n][k], At[m][k], acc[ai][bj][m][n], 0, 0, 0); __builtin_amdgcn_s_setprio(0); } while (0)
; #define PG8_WAIT_V(n) asm volatile("s_waitcnt vmcnt(" #n ")" ::: "memory")
; #define PG8_WAIT_L(n) asm volatile("s_waitcnt lgkmcnt(" #n ")" ::: "memory")
; #define PG8_BAR __builtin_amdgcn_s_barrier()
; #define PG8_SCHED __builtin_amdgcn_sched_barrier(0)
; template <class Epi, class Sched, bool ALIGN_EPI>
; __device__ __forceinline__ void gemm_phase(PG8_LAS unsigned char* lds, const Gemm g, const Sched& S, const Epi& E, const int tid) {
;     ...
;             PG8_LDB(B0, 0, 0); PG8_LDB(B1, 0, 1); PG8_SCHED; PG8_LDA(At, 0, 0); PG8_STAGE(PG8_SA(1, 1), a1 + hstepA, voffA);
;             PG8_WAIT_V(8); PG8_WAIT_L(0); PG8_BAR; PG8_MMA(0, 0, At, B0); PG8_MMA(0, 1, At, B1); PG8_BAR; PG8_SCHED;
;     ...
;             PG8_LDA(At, 1, 1); PG8_STAGE(PG8_SB(1, 0), b3, voffB); PG8_STAGE(PG8_SB(1, 1), b3 + hstepB, voffB); PG8_STAGE(PG8_SA(1, 0), a3, voffA);
;             PG8_WAIT_V(8); PG8_WAIT_L(0); PG8_BAR; PG8_MMA(1, 0, At, B0); PG8_MMA(1, 1, At, B1); PG8_BAR; PG8_SCHED;
	s_add_u32 s54, s52, 0x8000
	s_addc_u32 s55, s53, 0
	s_add_i32 s82, s82, s59
	s_mov_b32 m0, s82
	ds_read_b128 v[188:191], v210 offset:49152
	ds_read_b128 v[192:195], v210 offset:50176
	ds_read_b128 v[196:199], v210 offset:51200
	ds_read_b128 v[200:203], v210 offset:52224
	ds_read_b128 v[204:207], v210 offset:53248
	ds_read_b128 v[212:215], v210 offset:54272
	ds_read_b128 v[216:219], v210 offset:55296
	ds_read_b128 v[220:223], v210 offset:56320
	global_load_lds_dwordx4 v156, s[54:55]
	s_add_i32 m0, s82, 0x2000
	s_add_u32 s52, s52, 0xc000
	s_addc_u32 s53, s53, 0
	global_load_lds_dwordx4 v160, s[54:55]
	s_add_i32 s54, s83, s59
	s_mov_b32 m0, s54
	s_nop 0
	global_load_lds_dwordx4 v156, s[52:53]
	s_add_i32 m0, s54, 0x2000
	s_nop 0
	global_load_lds_dwordx4 v160, s[52:53]
	s_mov_b32 m0, s66
	s_nop 0
	global_load_lds_dwordx4 v154, s[12:13]
	s_mov_b32 m0, s67
	s_nop 0
	global_load_lds_dwordx4 v158, s[12:13]
	s_waitcnt vmcnt(8)
	s_waitcnt lgkmcnt(0)
	s_barrier
	v_mfma_f32_16x16x32_bf16 v[76:79], v[56:59], v[188:191], v[76:79]
	v_mfma_f32_16x16x32_bf16 v[72:75], v[64:67], v[188:191], v[72:75]
	v_mfma_f32_16x16x32_bf16 v[44:47], v[56:59], v[196:199], v[44:47]
	v_mfma_f32_16x16x32_bf16 v[40:43], v[64:67], v[196:199], v[40:43]
	v_mfma_f32_16x16x32_bf16 v[28:31], v[56:59], v[204:207], v[28:31]
	v_mfma_f32_16x16x32_bf16 v[24:27], v[64:67], v[204:207], v[24:27]
	v_mfma_f32_16x16x32_bf16 v[12:15], v[56:59], v[216:219], v[12:15]
	v_mfma_f32_16x16x32_bf16 v[8:11], v[64:67], v[216:219], v[8:11]
	v_mfma_f32_16x16x32_bf16 v[76:79], v[60:63], v[192:195], v[76:79]
	v_mfma_f32_16x16x32_bf16 v[72:75], v[68:71], v[192:195], v[72:75]
	v_mfma_f32_16x16x32_bf16 v[44:47], v[60:63], v[200:203], v[44:47]
	v_mfma_f32_16x16x32_bf16 v[40:43], v[68:71], v[200:203], v[40:43]
	v_mfma_f32_16x16x32_bf16 v[28:31], v[60:63], v[212:215], v[28:31]
	v_mfma_f32_16x16x32_bf16 v[24:27], v[68:71], v[212:215], v[24:27]
	v_mfma_f32_16x16x32_bf16 v[12:15], v[60:63], v[220:223], v[12:15]
	v_mfma_f32_16x16x32_bf16 v[8:11], v[68:71], v[220:223], v[8:11]
	v_mfma_f32_16x16x32_bf16 v[48:51], v[146:149], v[188:191], v[48:51]
	v_mfma_f32_16x16x32_bf16 v[60:63], v[150:153], v[192:195], v[48:51]
	v_mfma_f32_16x16x32_bf16 v[48:51], v[180:183], v[188:191], v[52:55]
	v_mfma_f32_16x16x32_bf16 v[36:39], v[146:149], v[196:199], v[36:39]
	v_mfma_f32_16x16x32_bf16 v[32:35], v[180:183], v[196:199], v[32:35]
	v_mfma_f32_16x16x32_bf16 v[20:23], v[146:149], v[204:207], v[20:23]
	v_mfma_f32_16x16x32_bf16 v[16:19], v[180:183], v[204:207], v[16:19]
	v_mfma_f32_16x16x32_bf16 v[4:7], v[146:149], v[216:219], v[4:7]
	v_mfma_f32_16x16x32_bf16 v[0:3], v[180:183], v[216:219], v[0:3]
	v_mfma_f32_16x16x32_bf16 v[56:59], v[184:187], v[192:195], v[48:51]
	v_mfma_f32_16x16x32_bf16 v[36:39], v[150:153], v[200:203], v[36:39]
	v_mfma_f32_16x16x32_bf16 v[32:35], v[184:187], v[200:203], v[32:35]
	v_mfma_f32_16x16x32_bf16 v[20:23], v[150:153], v[212:215], v[20:23]
	v_mfma_f32_16x16x32_bf16 v[16:19], v[184:187], v[212:215], v[16:19]
	v_mfma_f32_16x16x32_bf16 v[4:7], v[150:153], v[220:223], v[4:7]
	v_mfma_f32_16x16x32_bf16 v[0:3], v[184:187], v[220:223], v[0:3]
	s_barrier
	s_add_i32 s81, s81, 2
	s_add_u32 s10, s10, 0x10000
	s_addc_u32 s11, s11, 0
	s_add_u32 s79, s79, 0x10000
	s_addc_u32 s80, s80, 0
.LBB0_342:
	s_add_u32 s12, s10, 0x4000
	s_addc_u32 s13, s11, 0
	s_cmp_eq_u32 s81, 28
	s_cselect_b32 s54, s43, s12
	s_cselect_b32 s55, s9, s13
	s_cselect_b32 s52, s47, s79
	s_cselect_b32 s53, s45, s80
	s_add_u32 s12, s54, 0x8000
	s_addc_u32 s13, s55, 0
	s_add_i32 s82, 0, 0x10000
	s_add_i32 s84, 0, 0x14000
	ds_read_b128 v[48:51], v166
	ds_read_b128 v[52:55], v166 offset:1024
	ds_read_b128 v[64:67], v166 offset:2048
	ds_read_b128 v[68:71], v166 offset:3072
	ds_read_b128 v[146:149], v166 offset:16384
	ds_read_b128 v[150:153], v166 offset:17408
	ds_read_b128 v[180:183], v166 offset:18432
	ds_read_b128 v[184:187], v166 offset:19456
	s_add_i32 m0, s62, 0xc000
	ds_read_b128 v[188:191], v210
	ds_read_b128 v[192:195], v210 offset:1024
	ds_read_b128 v[196:199], v210 offset:2048
	ds_read_b128 v[200:203], v210 offset:3072
	ds_read_b128 v[204:207], v210 offset:4096
	ds_read_b128 v[212:215], v210 offset:5120
	ds_read_b128 v[216:219], v210 offset:6144
	ds_read_b128 v[220:223], v210 offset:7168
	global_load_lds_dwordx4 v176, s[10:11]
	s_add_i32 m0, s62, 0xe000
	s_nop 0
	global_load_lds_dwordx4 v178, s[10:11]
	s_waitcnt vmcnt(8)
	s_waitcnt lgkmcnt(0)
	s_barrier
	v_mfma_f32_16x16x32_bf16 v[142:145], v[48:51], v[188:191], v[142:145]
	v_mfma_f32_16x16x32_bf16 v[138:141], v[64:67], v[188:191], v[138:141]
	v_mfma_f32_16x16x32_bf16 v[124:127], v[48:51], v[196:199], v[124:127]
	v_mfma_f32_16x16x32_bf16 v[120:123], v[64:67], v[196:199], v[120:123]
	v_mfma_f32_16x16x32_bf16 v[108:111], v[48:51], v[204:207], v[108:111]
	v_mfma_f32_16x16x32_bf16 v[104:107], v[64:67], v[204:207], v[104:107]
	v_mfma_f32_16x16x32_bf16 v[92:95], v[48:51], v[216:219], v[92:95]
	v_mfma_f32_16x16x32_bf16 v[88:91], v[64:67], v[216:219], v[88:91]
	v_mfma_f32_16x16x32_bf16 v[142:145], v[52:55], v[192:195], v[142:145]
	v_mfma_f32_16x16x32_bf16 v[138:141], v[68:71], v[192:195], v[138:141]
	v_mfma_f32_16x16x32_bf16 v[124:127], v[52:55], v[200:203], v[124:127]
	v_mfma_f32_16x16x32_bf16 v[120:123], v[68:71], v[200:203], v[120:123]
	v_mfma_f32_16x16x32_bf16 v[108:111], v[52:55], v[212:215], v[108:111]
	v_mfma_f32_16x16x32_bf16 v[104:107], v[68:71], v[212:215], v[104:107]
	v_mfma_f32_16x16x32_bf16 v[92:95], v[52:55], v[220:223], v[92:95]
	v_mfma_f32_16x16x32_bf16 v[88:91], v[68:71], v[220:223], v[88:91]
	v_mfma_f32_16x16x32_bf16 v[134:137], v[146:149], v[188:191], v[134:137]
	v_mfma_f32_16x16x32_bf16 v[130:133], v[180:183], v[188:191], v[130:133]
	v_mfma_f32_16x16x32_bf16 v[116:119], v[146:149], v[196:199], v[116:119]
	v_mfma_f32_16x16x32_bf16 v[112:115], v[180:183], v[196:199], v[112:115]
	v_mfma_f32_16x16x32_bf16 v[100:103], v[146:149], v[204:207], v[100:103]
	v_mfma_f32_16x16x32_bf16 v[96:99], v[180:183], v[204:207], v[96:99]
	v_mfma_f32_16x16x32_bf16 v[84:87], v[146:149], v[216:219], v[84:87]
	v_mfma_f32_16x16x32_bf16 v[80:83], v[180:183], v[216:219], v[80:83]
	v_mfma_f32_16x16x32_bf16 v[134:137], v[150:153], v[192:195], v[134:137]
	v_mfma_f32_16x16x32_bf16 v[130:133], v[184:187], v[192:195], v[130:133]
	v_mfma_f32_16x16x32_bf16 v[116:119], v[150:153], v[200:203], v[116:119]
	v_mfma_f32_16x16x32_bf16 v[112:115], v[184:187], v[200:203], v[112:115]
	v_mfma_f32_16x16x32_bf16 v[100:103], v[150:153], v[212:215], v[100:103]
	v_mfma_f32_16x16x32_bf16 v[96:99], v[184:187], v[212:215], v[96:99]
	v_mfma_f32_16x16x32_bf16 v[84:87], v[150:153], v[220:223], v[84:87]
	v_mfma_f32_16x16x32_bf16 v[80:83], v[184:187], v[220:223], v[80:83]
	s_barrier
; #define PG8_STAGE(bufoff, gbase, voff) do { _Pragma("unroll") for (int _i = 0; _i < 2; ++_i) \
;         __builtin_amdgcn_global_load_lds((const unsigned*)((const char*)(gbase) + (voff)[_i]), (PG8_LAS unsigned*)(lds + (bufoff) + ldsw + _i * 8192), 16, 0, 0); } while (0)
; #define PG8_LDA(dst, b, h) do { _Pragma("unroll") for (int m = 0; m < 4; ++m) _Pragma("unroll") for (int k = 0; k < 2; ++k) dst[m][k] = *(const PG8_LAS bf16x8*)(lds + PG8_SA(b, h) + aoff + m * 2048 + k * 1024); } while (0)
; #define PG8_LDB(dst, b, h) do { _Pragma("unroll") for (int n = 0; n < 2; ++n) _Pragma("unroll") for (int k = 0; k < 2; ++k) dst[n][k] = *(const PG8_LAS bf16x8*)(lds + PG8_SB(b, h) + boff + n * 2048 + k * 1024); } while (0)
; #define PG8_MMA(ai, bj, At, Bt) do { __builtin_amdgcn_s_setprio(1); _Pragma("unroll") for (int m = 0; m < 4; ++m) _Pragma("unroll") for (int n = 0; n < 2; ++n) _Pragma("unroll") for (int k = 0; k < 2; ++k) \
;         acc[ai][bj][m][n] = __builtin_amdgcn_mfma_f32_16x16x32_bf16(Bt[n][k], At[m][k], acc[ai][bj][m][n], 0, 0, 0); __builtin_amdgcn_s_setprio(0); } while (0)
; #define PG8_WAIT_V(n) asm volatile("s_waitcnt vmcnt(" #n ")" ::: "memory")
; #define PG8_WAIT_L(n) asm volatile("s_waitcnt lgkmcnt(" #n ")" ::: "memory")
; #define PG8_BAR __builtin_amdgcn_s_barrier()
; #define PG8_SCHED __builtin_amdgcn_sched_barrier(0)
; template <class Epi, class Sched, bool ALIGN_EPI>
; __device__ __forceinline__ void gemm_phase(PG8_LAS unsigned char* lds, const Gemm g, const Sched& S, const Epi& E, const int tid) {
;     ...
;             PG8_LDA(At, 0, 1); PG8_STAGE(PG8_SB(0, 0), b2, voffB); PG8_STAGE(PG8_SB(0, 1), b2 + hstepB, voffB); PG8_STAGE(PG8_SA(0, 0), a2, voffA);
;             PG8_WAIT_V(8); PG8_WAIT_L(0); PG8_BAR; PG8_MMA(1, 0, At, B0); PG8_MMA(1, 1, At, B1); PG8_BAR; PG8_SCHED;
;             PG8_LDB(B0, 1, 0); PG8_LDB(B1, 1, 1); PG8_SCHED; PG8_LDA(At, 1, 0); PG8_STAGE(PG8_SA(0, 1), a2 + hstepA, voffA);
	s_add_i32 s82, s82, s59
	s_mov_b32 m0, s82
	ds_read_b128 v[188:191], v210 offset:16384
	ds_read_b128 v[192:195], v210 offset:17408
	ds_read_b128 v[196:199], v210 offset:18432
	ds_read_b128 v[200:203], v210 offset:19456
	ds_read_b128 v[204:207], v210 offset:20480
	ds_read_b128 v[212:215], v210 offset:21504
	ds_read_b128 v[216:219], v210 offset:22528
	ds_read_b128 v[220:223], v210 offset:23552
	global_load_lds_dwordx4 v156, s[52:53]
	s_add_i32 m0, s82, 0x2000
	s_add_u32 s82, s52, 0x4000
	s_addc_u32 s83, s53, 0
	s_add_i32 s84, s84, s59
	global_load_lds_dwordx4 v160, s[52:53]
	s_mov_b32 m0, s84
	s_nop 0
	global_load_lds_dwordx4 v156, s[82:83]
	s_add_i32 m0, s84, 0x2000
	s_nop 0
	global_load_lds_dwordx4 v160, s[82:83]
	s_mov_b32 m0, s62
	s_nop 0
	global_load_lds_dwordx4 v154, s[54:55]
	s_mov_b32 m0, s63
	s_nop 0
	global_load_lds_dwordx4 v158, s[54:55]
	s_waitcnt vmcnt(8)
	s_waitcnt lgkmcnt(0)
	s_barrier
	v_mfma_f32_16x16x32_bf16 v[76:79], v[48:51], v[188:191], v[76:79]
	v_mfma_f32_16x16x32_bf16 v[72:75], v[64:67], v[188:191], v[72:75]
	v_mfma_f32_16x16x32_bf16 v[44:47], v[48:51], v[196:199], v[44:47]
	v_mfma_f32_16x16x32_bf16 v[40:43], v[64:67], v[196:199], v[40:43]
	v_mfma_f32_16x16x32_bf16 v[28:31], v[48:51], v[204:207], v[28:31]
	v_mfma_f32_16x16x32_bf16 v[24:27], v[64:67], v[204:207], v[24:27]
	v_mfma_f32_16x16x32_bf16 v[12:15], v[48:51], v[216:219], v[12:15]
	v_mfma_f32_16x16x32_bf16 v[8:11], v[64:67], v[216:219], v[8:11]
	v_mfma_f32_16x16x32_bf16 v[76:79], v[52:55], v[192:195], v[76:79]
	v_mfma_f32_16x16x32_bf16 v[72:75], v[68:71], v[192:195], v[72:75]
	v_mfma_f32_16x16x32_bf16 v[44:47], v[52:55], v[200:203], v[44:47]
	v_mfma_f32_16x16x32_bf16 v[40:43], v[68:71], v[200:203], v[40:43]
	v_mfma_f32_16x16x32_bf16 v[28:31], v[52:55], v[212:215], v[28:31]
	v_mfma_f32_16x16x32_bf16 v[24:27], v[68:71], v[212:215], v[24:27]
	v_mfma_f32_16x16x32_bf16 v[12:15], v[52:55], v[220:223], v[12:15]
	v_mfma_f32_16x16x32_bf16 v[8:11], v[68:71], v[220:223], v[8:11]
	v_mfma_f32_16x16x32_bf16 v[36:39], v[146:149], v[196:199], v[36:39]
	v_mfma_f32_16x16x32_bf16 v[32:35], v[180:183], v[196:199], v[32:35]
	v_mfma_f32_16x16x32_bf16 v[20:23], v[146:149], v[204:207], v[20:23]
	v_mfma_f32_16x16x32_bf16 v[16:19], v[180:183], v[204:207], v[16:19]
	v_mfma_f32_16x16x32_bf16 v[4:7], v[146:149], v[216:219], v[4:7]
	v_mfma_f32_16x16x32_bf16 v[0:3], v[180:183], v[216:219], v[0:3]
	v_mfma_f32_16x16x32_bf16 v[48:51], v[146:149], v[188:191], v[60:63]
	v_mfma_f32_16x16x32_bf16 v[52:55], v[180:183], v[188:191], v[56:59]
	v_mfma_f32_16x16x32_bf16 v[36:39], v[150:153], v[200:203], v[36:39]
	v_mfma_f32_16x16x32_bf16 v[32:35], v[184:187], v[200:203], v[32:35]
	v_mfma_f32_16x16x32_bf16 v[20:23], v[150:153], v[212:215], v[20:23]
	v_mfma_f32_16x16x32_bf16 v[16:19], v[184:187], v[212:215], v[16:19]
	v_mfma_f32_16x16x32_bf16 v[4:7], v[150:153], v[220:223], v[4:7]
	v_mfma_f32_16x16x32_bf16 v[0:3], v[184:187], v[220:223], v[0:3]
	v_mfma_f32_16x16x32_bf16 v[48:51], v[150:153], v[192:195], v[48:51]
	v_mfma_f32_16x16x32_bf16 v[52:55], v[184:187], v[192:195], v[52:55]
	s_barrier
	s_add_i32 s82, 0, 0x18000
	s_add_i32 s83, 0, 0x1c000
	ds_read_b128 v[56:59], v166 offset:32768
	ds_read_b128 v[60:63], v166 offset:33792
	ds_read_b128 v[64:67], v166 offset:34816
	ds_read_b128 v[68:71], v166 offset:35840
	ds_read_b128 v[146:149], v166 offset:49152
	ds_read_b128 v[150:153], v166 offset:50176
	ds_read_b128 v[180:183], v166 offset:51200
	ds_read_b128 v[184:187], v166 offset:52224
	s_add_u32 s54, s54, 0x4000
	s_addc_u32 s55, s55, 0
	s_mov_b32 m0, s64
	ds_read_b128 v[188:191], v210 offset:32768
	ds_read_b128 v[192:195], v210 offset:33792
	ds_read_b128 v[196:199], v210 offset:34816
	ds_read_b128 v[200:203], v210 offset:35840
	ds_read_b128 v[204:207], v210 offset:36864
	ds_read_b128 v[212:215], v210 offset:37888
	ds_read_b128 v[216:219], v210 offset:38912
	ds_read_b128 v[220:223], v210 offset:39936
	global_load_lds_dwordx4 v154, s[54:55]
	s_mov_b32 m0, s65
	s_nop 0
	global_load_lds_dwordx4 v158, s[54:55]
	s_waitcnt vmcnt(8)
	s_waitcnt lgkmcnt(0)
	s_barrier
; #define PG8_STAGE(bufoff, gbase, voff) do { _Pragma("unroll") for (int _i = 0; _i < 2; ++_i) \
;         __builtin_amdgcn_global_load_lds((const unsigned*)((const char*)(gbase) + (voff)[_i]), (PG8_LAS unsigned*)(lds + (bufoff) + ldsw + _i * 8192), 16, 0, 0); } while (0)
; #define PG8_LDA(dst, b, h) do { _Pragma("unroll") for (int m = 0; m < 4; ++m) _Pragma("unroll") for (int k = 0; k < 2; ++k) dst[m][k] = *(const PG8_LAS bf16x8*)(lds + PG8_SA(b, h) + aoff + m * 2048 + k * 1024); } while (0)
; #define PG8_MMA(ai, bj, At, Bt) do { __builtin_amdgcn_s_setprio(1); _Pragma("unroll") for (int m = 0; m < 4; ++m) _Pragma("unroll") for (int n = 0; n < 2; ++n) _Pragma("unroll") for (int k = 0; k < 2; ++k) \
;         acc[ai][bj][m][n] = __builtin_amdgcn_mfma_f32_16x16x32_bf16(Bt[n][k], At[m][k], acc[ai][bj][m][n], 0, 0, 0); __builtin_amdgcn_s_setprio(0); } while (0)
; #define PG8_WAIT_V(n) asm volatile("s_waitcnt vmcnt(" #n ")" ::: "memory")
; #define PG8_WAIT_L(n) asm volatile("s_waitcnt lgkmcnt(" #n ")" ::: "memory")
; #define PG8_BAR __builtin_amdgcn_s_barrier()
; #define PG8_SCHED __builtin_amdgcn_sched_barrier(0)
; template <class Epi, class Sched, bool ALIGN_EPI>
; __device__ __forceinline__ void gemm_phase(PG8_LAS unsigned char* lds, const Gemm g, const Sched& S, const Epi& E, const int tid) {
;     ...
;             PG8_WAIT_V(8); PG8_WAIT_L(0); PG8_BAR; PG8_MMA(0, 0, At, B0); PG8_MMA(0, 1, At, B1); PG8_BAR; PG8_SCHED;
;             PG8_LDA(At, 1, 1); PG8_STAGE(PG8_SB(1, 0), b3, voffB); PG8_STAGE(PG8_SB(1, 1), b3 + hstepB, voffB); PG8_STAGE(PG8_SA(1, 0), a3, voffA);
;             PG8_WAIT_V(8); PG8_WAIT_L(0); PG8_BAR; PG8_MMA(1, 0, At, B0); PG8_MMA(1, 1, At, B1); PG8_BAR; PG8_SCHED;
;         }
;         if constexpr (ALIGN_EPI) { if (wr == 0) PG8_BAR; }
	v_mfma_f32_16x16x32_bf16 v[142:145], v[56:59], v[188:191], v[142:145]
	v_mfma_f32_16x16x32_bf16 v[138:141], v[64:67], v[188:191], v[138:141]
	v_mfma_f32_16x16x32_bf16 v[124:127], v[56:59], v[196:199], v[124:127]
	v_mfma_f32_16x16x32_bf16 v[120:123], v[64:67], v[196:199], v[120:123]
	v_mfma_f32_16x16x32_bf16 v[108:111], v[56:59], v[204:207], v[108:111]
	v_mfma_f32_16x16x32_bf16 v[104:107], v[64:67], v[204:207], v[104:107]
	v_mfma_f32_16x16x32_bf16 v[92:95], v[56:59], v[216:219], v[92:95]
	v_mfma_f32_16x16x32_bf16 v[88:91], v[64:67], v[216:219], v[88:91]
	v_mfma_f32_16x16x32_bf16 v[142:145], v[60:63], v[192:195], v[142:145]
	v_mfma_f32_16x16x32_bf16 v[138:141], v[68:71], v[192:195], v[138:141]
	v_mfma_f32_16x16x32_bf16 v[124:127], v[60:63], v[200:203], v[124:127]
	v_mfma_f32_16x16x32_bf16 v[120:123], v[68:71], v[200:203], v[120:123]
	v_mfma_f32_16x16x32_bf16 v[108:111], v[60:63], v[212:215], v[108:111]
	v_mfma_f32_16x16x32_bf16 v[104:107], v[68:71], v[212:215], v[104:107]
	v_mfma_f32_16x16x32_bf16 v[92:95], v[60:63], v[220:223], v[92:95]
	v_mfma_f32_16x16x32_bf16 v[88:91], v[68:71], v[220:223], v[88:91]
	v_mfma_f32_16x16x32_bf16 v[134:137], v[146:149], v[188:191], v[134:137]
	v_mfma_f32_16x16x32_bf16 v[130:133], v[180:183], v[188:191], v[130:133]
	v_mfma_f32_16x16x32_bf16 v[116:119], v[146:149], v[196:199], v[116:119]
	v_mfma_f32_16x16x32_bf16 v[112:115], v[180:183], v[196:199], v[112:115]
	v_mfma_f32_16x16x32_bf16 v[100:103], v[146:149], v[204:207], v[100:103]
	v_mfma_f32_16x16x32_bf16 v[96:99], v[180:183], v[204:207], v[96:99]
	v_mfma_f32_16x16x32_bf16 v[84:87], v[146:149], v[216:219], v[84:87]
	v_mfma_f32_16x16x32_bf16 v[80:83], v[180:183], v[216:219], v[80:83]
	v_mfma_f32_16x16x32_bf16 v[134:137], v[150:153], v[192:195], v[134:137]
	v_mfma_f32_16x16x32_bf16 v[130:133], v[184:187], v[192:195], v[130:133]
	v_mfma_f32_16x16x32_bf16 v[116:119], v[150:153], v[200:203], v[116:119]
	v_mfma_f32_16x16x32_bf16 v[112:115], v[184:187], v[200:203], v[112:115]
	v_mfma_f32_16x16x32_bf16 v[100:103], v[150:153], v[212:215], v[100:103]
	v_mfma_f32_16x16x32_bf16 v[96:99], v[184:187], v[212:215], v[96:99]
	v_mfma_f32_16x16x32_bf16 v[84:87], v[150:153], v[220:223], v[84:87]
	v_mfma_f32_16x16x32_bf16 v[80:83], v[184:187], v[220:223], v[80:83]
	s_barrier
	s_add_u32 s54, s52, 0x8000
	s_addc_u32 s55, s53, 0
	s_add_i32 s82, s82, s59
	s_mov_b32 m0, s82
	ds_read_b128 v[188:191], v210 offset:49152
	ds_read_b128 v[192:195], v210 offset:50176
	ds_read_b128 v[196:199], v210 offset:51200
	ds_read_b128 v[200:203], v210 offset:52224
	ds_read_b128 v[204:207], v210 offset:53248
	ds_read_b128 v[212:215], v210 offset:54272
	ds_read_b128 v[216:219], v210 offset:55296
	ds_read_b128 v[220:223], v210 offset:56320
	global_load_lds_dwordx4 v156, s[54:55]
	s_add_i32 m0, s82, 0x2000
	s_add_u32 s52, s52, 0xc000
	s_addc_u32 s53, s53, 0
	global_load_lds_dwordx4 v160, s[54:55]
	s_add_i32 s54, s83, s59
	s_mov_b32 m0, s54
	s_nop 0
	global_load_lds_dwordx4 v156, s[52:53]
	s_add_i32 m0, s54, 0x2000
	s_nop 0
	global_load_lds_dwordx4 v160, s[52:53]
	s_mov_b32 m0, s66
	s_nop 0
	global_load_lds_dwordx4 v154, s[12:13]
	s_mov_b32 m0, s67
	s_nop 0
	global_load_lds_dwordx4 v158, s[12:13]
	s_waitcnt vmcnt(8)
	s_waitcnt lgkmcnt(0)
	s_barrier
	v_mfma_f32_16x16x32_bf16 v[76:79], v[56:59], v[188:191], v[76:79]
	v_mfma_f32_16x16x32_bf16 v[72:75], v[64:67], v[188:191], v[72:75]
	v_mfma_f32_16x16x32_bf16 v[44:47], v[56:59], v[196:199], v[44:47]
	v_mfma_f32_16x16x32_bf16 v[40:43], v[64:67], v[196:199], v[40:43]
	v_mfma_f32_16x16x32_bf16 v[28:31], v[56:59], v[204:207], v[28:31]
	v_mfma_f32_16x16x32_bf16 v[24:27], v[64:67], v[204:207], v[24:27]
	v_mfma_f32_16x16x32_bf16 v[12:15], v[56:59], v[216:219], v[12:15]
	v_mfma_f32_16x16x32_bf16 v[8:11], v[64:67], v[216:219], v[8:11]
	v_mfma_f32_16x16x32_bf16 v[76:79], v[60:63], v[192:195], v[76:79]
	v_mfma_f32_16x16x32_bf16 v[72:75], v[68:71], v[192:195], v[72:75]
	v_mfma_f32_16x16x32_bf16 v[44:47], v[60:63], v[200:203], v[44:47]
	v_mfma_f32_16x16x32_bf16 v[40:43], v[68:71], v[200:203], v[40:43]
	v_mfma_f32_16x16x32_bf16 v[28:31], v[60:63], v[212:215], v[28:31]
	v_mfma_f32_16x16x32_bf16 v[24:27], v[68:71], v[212:215], v[24:27]
	v_mfma_f32_16x16x32_bf16 v[12:15], v[60:63], v[220:223], v[12:15]
	v_mfma_f32_16x16x32_bf16 v[8:11], v[68:71], v[220:223], v[8:11]
	v_mfma_f32_16x16x32_bf16 v[48:51], v[146:149], v[188:191], v[48:51]
	v_mfma_f32_16x16x32_bf16 v[60:63], v[150:153], v[192:195], v[48:51]
	v_mfma_f32_16x16x32_bf16 v[48:51], v[180:183], v[188:191], v[52:55]
	v_mfma_f32_16x16x32_bf16 v[36:39], v[146:149], v[196:199], v[36:39]
	v_mfma_f32_16x16x32_bf16 v[32:35], v[180:183], v[196:199], v[32:35]
	v_mfma_f32_16x16x32_bf16 v[20:23], v[146:149], v[204:207], v[20:23]
	v_mfma_f32_16x16x32_bf16 v[16:19], v[180:183], v[204:207], v[16:19]
	v_mfma_f32_16x16x32_bf16 v[4:7], v[146:149], v[216:219], v[4:7]
	v_mfma_f32_16x16x32_bf16 v[0:3], v[180:183], v[216:219], v[0:3]
	v_mfma_f32_16x16x32_bf16 v[56:59], v[184:187], v[192:195], v[48:51]
	v_mfma_f32_16x16x32_bf16 v[36:39], v[150:153], v[200:203], v[36:39]
	v_mfma_f32_16x16x32_bf16 v[32:35], v[184:187], v[200:203], v[32:35]
	v_mfma_f32_16x16x32_bf16 v[20:23], v[150:153], v[212:215], v[20:23]
	v_mfma_f32_16x16x32_bf16 v[16:19], v[184:187], v[212:215], v[16:19]
	v_mfma_f32_16x16x32_bf16 v[4:7], v[150:153], v[220:223], v[4:7]
	v_mfma_f32_16x16x32_bf16 v[0:3], v[184:187], v[220:223], v[0:3]
	s_barrier
	s_add_i32 s81, s81, 2
	s_add_u32 s10, s10, 0x10000
	s_addc_u32 s11, s11, 0
	s_add_u32 s79, s79, 0x10000
	s_addc_u32 s80, s80, 0
	s_cmp_gt_u32 s81, 29
	s_cbranch_scc0 .LBB0_342
	s_and_b64 vcc, exec, s[34:35]
	s_cbranch_vccz .LBB0_345
	s_barrier

; #define PG8_WAIT_V(n) asm volatile("s_waitcnt vmcnt(" #n ")" ::: "memory")
; #define PG8_BAR __builtin_amdgcn_s_barrier()
; template <class Epi, class Sched, bool ALIGN_EPI>
; __device__ __forceinline__ void gemm_phase(PG8_LAS unsigned char* lds, const Gemm g, const Sched& S, const Epi& E, const int tid) {
;     ...
;     PG8_WAIT_V(0);
;     if constexpr (!ALIGN_EPI) { if (wr == 0) PG8_BAR; }
;     PG8_BAR;
.LBB0_499:
	s_setprio 0
	s_waitcnt vmcnt(0)
	s_mov_b32 s76, 0xffff0000
	s_mov_b32 s77, 0xc2fc0000
	s_movk_i32 s78, 0xffef
	s_mov_b32 s65, s91
	s_barrier

; #define PG8_STAGE(bufoff, gbase, voff) do { _Pragma("unroll") for (int _i = 0; _i < 2; ++_i) \
;         __builtin_amdgcn_global_load_lds((const unsigned*)((const char*)(gbase) + (voff)[_i]), (PG8_LAS unsigned*)(lds + (bufoff) + ldsw + _i * 8192), 16, 0, 0); } while (0)
; #define PG8_LDA(dst, b, h) do { _Pragma("unroll") for (int m = 0; m < 4; ++m) _Pragma("unroll") for (int k = 0; k < 2; ++k) dst[m][k] = *(const PG8_LAS bf16x8*)(lds + PG8_SA(b, h) + aoff + m * 2048 + k * 1024); } while (0)
; #define PG8_LDB(dst, b, h) do { _Pragma("unroll") for (int n = 0; n < 2; ++n) _Pragma("unroll") for (int k = 0; k < 2; ++k) dst[n][k] = *(const PG8_LAS bf16x8*)(lds + PG8_SB(b, h) + boff + n * 2048 + k * 1024); } while (0)
; #define PG8_MMA(ai, bj, At, Bt) do { __builtin_amdgcn_s_setprio(1); _Pragma("unroll") for (int m = 0; m < 4; ++m) _Pragma("unroll") for (int n = 0; n < 2; ++n) _Pragma("unroll") for (int k = 0; k < 2; ++k) \
;         acc[ai][bj][m][n] = __builtin_amdgcn_mfma_f32_16x16x32_bf16(Bt[n][k], At[m][k], acc[ai][bj][m][n], 0, 0, 0); __builtin_amdgcn_s_setprio(0); } while (0)
; #define PG8_BAR __builtin_amdgcn_s_barrier()
; template <class Epi, class Sched, bool ALIGN_EPI>
; __device__ __forceinline__ void gemm_phase(PG8_LAS unsigned char* lds, const Gemm g, const Sched& S, const Epi& E, const int tid) {
;     ...
;         const bool has_next = S.next(ui + 1, nxt);
;         const char* nA = has_next ? (const char*)g.A + (size_t)nxt.pm * tstepA + PG8_ACOL(nxt) : cA; const char* nB = has_next ? (const char*)g.Bt + (size_t)nxt.pn * tstepB : cB;
;         for (int t = 0; t < nt; t += 2) {
;             const bool last = (t == nt - 2);
;             const char* a1 = cA + (size_t)(t + 1) * kstepA;
;             const char* a2 = last ? nA : cA + (size_t)(t + 2) * kstepA; const char* b2 = last ? nB : cB + (size_t)(t + 2) * kstepB;
;             const char* a3 = a2 + kstepA; const char* b3 = b2 + kstepB;
;             if (last && has_next) S.a_ready(nxt);
;             PG8_LDB(B0, 0, 0); PG8_LDB(B1, 0, 1); PG8_SCHED; PG8_LDA(At, 0, 0); PG8_STAGE(PG8_SA(1, 1), a1 + hstepA, voffA);
;             PG8_WAIT_V(8); PG8_WAIT_L(0); PG8_BAR; PG8_MMA(0, 0, At, B0); PG8_MMA(0, 1, At, B1); PG8_BAR; PG8_SCHED;
;             PG8_LDA(At, 0, 1); PG8_STAGE(PG8_SB(0, 0), b2, voffB); PG8_STAGE(PG8_SB(0, 1), b2 + hstepB, voffB); PG8_STAGE(PG8_SA(0, 0), a2, voffA);
.LBB0_1395:
	s_add_u32 s50, s18, s68
	s_addc_u32 s51, s19, s69
	s_add_u32 s52, s20, 0x10000
	s_addc_u32 s53, s21, 0
	s_mov_b64 s[20:21], 0
	v_add_u32_e32 v192, 0x10000, v195
	s_add_u32 s54, s20, 1
	s_addc_u32 s55, s21, 0
	s_add_u32 s22, s20, 2
	s_addc_u32 s23, s21, 0
	s_lshl_b64 s[24:25], s[22:23], s44
	s_add_u32 s21, s18, s24
	s_addc_u32 s24, s19, s25
	s_cmp_eq_u32 s45, s20
	s_cselect_b32 s26, s8, s21
	s_cselect_b32 s27, s9, s24
	s_cselect_b32 s24, s16, s52
	s_cselect_b32 s25, s17, s53
	s_add_u32 s20, s26, s38
	s_addc_u32 s21, s27, 0
	s_add_i32 s56, 0, 0x10000
	s_add_i32 s57, 0, 0x14000
	ds_read_b128 v[88:91], v192
	ds_read_b128 v[92:95], v192 offset:1024
	ds_read_b128 v[100:103], v192 offset:2048
	ds_read_b128 v[108:111], v192 offset:3072
	ds_read_b128 v[146:149], v192 offset:16384
	ds_read_b128 v[150:153], v192 offset:17408
	ds_read_b128 v[154:157], v192 offset:18432
	ds_read_b128 v[158:161], v192 offset:19456
	s_lshl_b64 s[54:55], s[54:55], s44
	s_add_u32 s54, s50, s54
	s_addc_u32 s55, s51, s55
	s_add_i32 m0, s31, 0xc000
	ds_read_b128 v[162:165], v185
	ds_read_b128 v[166:169], v185 offset:1024
	ds_read_b128 v[172:175], v185 offset:2048
	ds_read_b128 v[188:191], v185 offset:3072
	ds_read_b128 v[196:199], v185 offset:4096
	ds_read_b128 v[200:203], v185 offset:5120
	ds_read_b128 v[204:207], v185 offset:6144
	ds_read_b128 v[208:211], v185 offset:7168
	global_load_lds_dwordx4 v176, s[54:55]
	s_add_i32 m0, s31, 0xe000
	s_nop 0
	global_load_lds_dwordx4 v180, s[54:55]
	s_waitcnt vmcnt(8)
	s_waitcnt lgkmcnt(0)
	s_and_b64 vcc, exec, s[14:15]
	s_cbranch_vccnz .Lsprio_2
	s_setprio 1
.Lsprio_2:
	s_barrier
	v_mfma_f32_16x16x32_bf16 v[142:145], v[88:91], v[162:165], 0
	v_mfma_f32_16x16x32_bf16 v[138:141], v[100:103], v[162:165], 0
	v_mfma_f32_16x16x32_bf16 v[124:127], v[88:91], v[172:175], 0
	v_mfma_f32_16x16x32_bf16 v[120:123], v[100:103], v[172:175], 0
	v_mfma_f32_16x16x32_bf16 v[104:107], v[88:91], v[196:199], 0
	v_mfma_f32_16x16x32_bf16 v[96:99], v[100:103], v[196:199], 0
	v_mfma_f32_16x16x32_bf16 v[76:79], v[88:91], v[204:207], 0
	v_mfma_f32_16x16x32_bf16 v[72:75], v[100:103], v[204:207], 0
	v_mfma_f32_16x16x32_bf16 v[142:145], v[92:95], v[166:169], v[142:145]
	v_mfma_f32_16x16x32_bf16 v[138:141], v[108:111], v[166:169], v[138:141]
	v_mfma_f32_16x16x32_bf16 v[124:127], v[92:95], v[188:191], v[124:127]
	v_mfma_f32_16x16x32_bf16 v[120:123], v[108:111], v[188:191], v[120:123]
	v_mfma_f32_16x16x32_bf16 v[104:107], v[92:95], v[200:203], v[104:107]
	v_mfma_f32_16x16x32_bf16 v[96:99], v[108:111], v[200:203], v[96:99]
	v_mfma_f32_16x16x32_bf16 v[76:79], v[92:95], v[208:211], v[76:79]
	v_mfma_f32_16x16x32_bf16 v[72:75], v[108:111], v[208:211], v[72:75]
	v_mfma_f32_16x16x32_bf16 v[134:137], v[146:149], v[162:165], 0
	v_mfma_f32_16x16x32_bf16 v[130:133], v[154:157], v[162:165], 0
	v_mfma_f32_16x16x32_bf16 v[116:119], v[146:149], v[172:175], 0
	v_mfma_f32_16x16x32_bf16 v[112:115], v[154:157], v[172:175], 0
	v_mfma_f32_16x16x32_bf16 v[84:87], v[146:149], v[196:199], 0
	v_mfma_f32_16x16x32_bf16 v[80:83], v[154:157], v[196:199], 0
	v_mfma_f32_16x16x32_bf16 v[68:71], v[146:149], v[204:207], 0
	v_mfma_f32_16x16x32_bf16 v[64:67], v[154:157], v[204:207], 0
	v_mfma_f32_16x16x32_bf16 v[134:137], v[150:153], v[166:169], v[134:137]
	v_mfma_f32_16x16x32_bf16 v[130:133], v[158:161], v[166:169], v[130:133]
	v_mfma_f32_16x16x32_bf16 v[116:119], v[150:153], v[188:191], v[116:119]
	v_mfma_f32_16x16x32_bf16 v[112:115], v[158:161], v[188:191], v[112:115]
	v_mfma_f32_16x16x32_bf16 v[84:87], v[150:153], v[200:203], v[84:87]
	v_mfma_f32_16x16x32_bf16 v[80:83], v[158:161], v[200:203], v[80:83]
	v_mfma_f32_16x16x32_bf16 v[68:71], v[150:153], v[208:211], v[68:71]
	v_mfma_f32_16x16x32_bf16 v[64:67], v[158:161], v[208:211], v[64:67]
	s_barrier
	s_add_i32 s54, s56, s30
	s_mov_b32 m0, s54
	ds_read_b128 v[162:165], v185 offset:16384
	ds_read_b128 v[166:169], v185 offset:17408
	ds_read_b128 v[172:175], v185 offset:18432
	ds_read_b128 v[188:191], v185 offset:19456
	ds_read_b128 v[196:199], v185 offset:20480
	ds_read_b128 v[200:203], v185 offset:21504
	ds_read_b128 v[204:207], v185 offset:22528
	ds_read_b128 v[208:211], v185 offset:23552
	global_load_lds_dwordx4 v178, s[24:25]
	s_add_i32 m0, s54, 0x2000
	s_add_u32 s54, s24, 0x4000
	s_addc_u32 s55, s25, 0
	s_add_i32 s56, s57, s30
	global_load_lds_dwordx4 v182, s[24:25]
	s_mov_b32 m0, s56
	s_nop 0
	global_load_lds_dwordx4 v178, s[54:55]
	s_add_i32 m0, s56, 0x2000
	s_nop 0
	global_load_lds_dwordx4 v182, s[54:55]
	s_mov_b32 m0, s31
	s_nop 0
	global_load_lds_dwordx4 v176, s[26:27]
	s_mov_b32 m0, s33
	s_nop 0
	global_load_lds_dwordx4 v180, s[26:27]
	s_waitcnt vmcnt(8)
	s_waitcnt lgkmcnt(0)
	s_barrier
; #define PG8_STAGE(bufoff, gbase, voff) do { _Pragma("unroll") for (int _i = 0; _i < 2; ++_i) \
;         __builtin_amdgcn_global_load_lds((const unsigned*)((const char*)(gbase) + (voff)[_i]), (PG8_LAS unsigned*)(lds + (bufoff) + ldsw + _i * 8192), 16, 0, 0); } while (0)
; #define PG8_LDA(dst, b, h) do { _Pragma("unroll") for (int m = 0; m < 4; ++m) _Pragma("unroll") for (int k = 0; k < 2; ++k) dst[m][k] = *(const PG8_LAS bf16x8*)(lds + PG8_SA(b, h) + aoff + m * 2048 + k * 1024); } while (0)
; #define PG8_LDB(dst, b, h) do { _Pragma("unroll") for (int n = 0; n < 2; ++n) _Pragma("unroll") for (int k = 0; k < 2; ++k) dst[n][k] = *(const PG8_LAS bf16x8*)(lds + PG8_SB(b, h) + boff + n * 2048 + k * 1024); } while (0)
; #define PG8_MMA(ai, bj, At, Bt) do { __builtin_amdgcn_s_setprio(1); _Pragma("unroll") for (int m = 0; m < 4; ++m) _Pragma("unroll") for (int n = 0; n < 2; ++n) _Pragma("unroll") for (int k = 0; k < 2; ++k) \
;         acc[ai][bj][m][n] = __builtin_amdgcn_mfma_f32_16x16x32_bf16(Bt[n][k], At[m][k], acc[ai][bj][m][n], 0, 0, 0); __builtin_amdgcn_s_setprio(0); } while (0)
; #define PG8_WAIT_V(n) asm volatile("s_waitcnt vmcnt(" #n ")" ::: "memory")
; #define PG8_WAIT_L(n) asm volatile("s_waitcnt lgkmcnt(" #n ")" ::: "memory")
; #define PG8_BAR __builtin_amdgcn_s_barrier()
; #define PG8_SCHED __builtin_amdgcn_sched_barrier(0)
; template <class Epi, class Sched, bool ALIGN_EPI>
; __device__ __forceinline__ void gemm_phase(PG8_LAS unsigned char* lds, const Gemm g, const Sched& S, const Epi& E, const int tid) {
;     ...
;             PG8_WAIT_V(8); PG8_WAIT_L(0); PG8_BAR; PG8_MMA(1, 0, At, B0); PG8_MMA(1, 1, At, B1); PG8_BAR; PG8_SCHED;
;             PG8_LDB(B0, 1, 0); PG8_LDB(B1, 1, 1); PG8_SCHED; PG8_LDA(At, 1, 0); PG8_STAGE(PG8_SA(0, 1), a2 + hstepA, voffA);
;             PG8_WAIT_V(8); PG8_WAIT_L(0); PG8_BAR; PG8_MMA(0, 0, At, B0); PG8_MMA(0, 1, At, B1); PG8_BAR; PG8_SCHED;
;             PG8_LDA(At, 1, 1); PG8_STAGE(PG8_SB(1, 0), b3, voffB); PG8_STAGE(PG8_SB(1, 1), b3 + hstepB, voffB); PG8_STAGE(PG8_SA(1, 0), a3, voffA);
	v_mfma_f32_16x16x32_bf16 v[60:63], v[88:91], v[162:165], 0
	v_mfma_f32_16x16x32_bf16 v[56:59], v[100:103], v[162:165], 0
	v_mfma_f32_16x16x32_bf16 v[44:47], v[88:91], v[172:175], 0
	v_mfma_f32_16x16x32_bf16 v[40:43], v[100:103], v[172:175], 0
	v_mfma_f32_16x16x32_bf16 v[28:31], v[88:91], v[196:199], 0
	v_mfma_f32_16x16x32_bf16 v[24:27], v[100:103], v[196:199], 0
	v_mfma_f32_16x16x32_bf16 v[12:15], v[88:91], v[204:207], 0
	v_mfma_f32_16x16x32_bf16 v[8:11], v[100:103], v[204:207], 0
	v_mfma_f32_16x16x32_bf16 v[60:63], v[92:95], v[166:169], v[60:63]
	v_mfma_f32_16x16x32_bf16 v[56:59], v[108:111], v[166:169], v[56:59]
	v_mfma_f32_16x16x32_bf16 v[44:47], v[92:95], v[188:191], v[44:47]
	v_mfma_f32_16x16x32_bf16 v[40:43], v[108:111], v[188:191], v[40:43]
	v_mfma_f32_16x16x32_bf16 v[28:31], v[92:95], v[200:203], v[28:31]
	v_mfma_f32_16x16x32_bf16 v[24:27], v[108:111], v[200:203], v[24:27]
	v_mfma_f32_16x16x32_bf16 v[12:15], v[92:95], v[208:211], v[12:15]
	v_mfma_f32_16x16x32_bf16 v[8:11], v[108:111], v[208:211], v[8:11]
	v_mfma_f32_16x16x32_bf16 v[52:55], v[146:149], v[162:165], 0
	v_mfma_f32_16x16x32_bf16 v[48:51], v[154:157], v[162:165], 0
	v_mfma_f32_16x16x32_bf16 v[36:39], v[146:149], v[172:175], 0
	v_mfma_f32_16x16x32_bf16 v[32:35], v[154:157], v[172:175], 0
	v_mfma_f32_16x16x32_bf16 v[20:23], v[146:149], v[196:199], 0
	v_mfma_f32_16x16x32_bf16 v[16:19], v[154:157], v[196:199], 0
	v_mfma_f32_16x16x32_bf16 v[4:7], v[146:149], v[204:207], 0
	v_mfma_f32_16x16x32_bf16 v[0:3], v[154:157], v[204:207], 0
	v_mfma_f32_16x16x32_bf16 v[52:55], v[150:153], v[166:169], v[52:55]
	v_mfma_f32_16x16x32_bf16 v[48:51], v[158:161], v[166:169], v[48:51]
	v_mfma_f32_16x16x32_bf16 v[36:39], v[150:153], v[188:191], v[36:39]
	v_mfma_f32_16x16x32_bf16 v[32:35], v[158:161], v[188:191], v[32:35]
	v_mfma_f32_16x16x32_bf16 v[20:23], v[150:153], v[200:203], v[20:23]
	v_mfma_f32_16x16x32_bf16 v[16:19], v[158:161], v[200:203], v[16:19]
	v_mfma_f32_16x16x32_bf16 v[4:7], v[150:153], v[208:211], v[4:7]
	v_mfma_f32_16x16x32_bf16 v[0:3], v[158:161], v[208:211], v[0:3]
	s_barrier
	s_add_i32 s54, 0, 0x18000
	s_add_i32 s55, 0, 0x1c000
	ds_read_b128 v[88:91], v192 offset:32768
	ds_read_b128 v[92:95], v192 offset:33792
	ds_read_b128 v[100:103], v192 offset:34816
	ds_read_b128 v[108:111], v192 offset:35840
	ds_read_b128 v[146:149], v192 offset:49152
	ds_read_b128 v[150:153], v192 offset:50176
	ds_read_b128 v[154:157], v192 offset:51200
	ds_read_b128 v[158:161], v192 offset:52224
	s_add_u32 s26, s26, s68
	s_addc_u32 s27, s27, s69
	s_mov_b32 m0, s34
	ds_read_b128 v[162:165], v185 offset:32768
	ds_read_b128 v[166:169], v185 offset:33792
	ds_read_b128 v[172:175], v185 offset:34816
	ds_read_b128 v[188:191], v185 offset:35840
	ds_read_b128 v[196:199], v185 offset:36864
	ds_read_b128 v[200:203], v185 offset:37888
	ds_read_b128 v[204:207], v185 offset:38912
	ds_read_b128 v[208:211], v185 offset:39936
	global_load_lds_dwordx4 v176, s[26:27]
	s_mov_b32 m0, s35
	s_nop 0
	global_load_lds_dwordx4 v180, s[26:27]
	s_waitcnt vmcnt(8)
	s_waitcnt lgkmcnt(0)
	s_barrier
	v_mfma_f32_16x16x32_bf16 v[142:145], v[88:91], v[162:165], v[142:145]
	v_mfma_f32_16x16x32_bf16 v[138:141], v[100:103], v[162:165], v[138:141]
	v_mfma_f32_16x16x32_bf16 v[124:127], v[88:91], v[172:175], v[124:127]
	v_mfma_f32_16x16x32_bf16 v[120:123], v[100:103], v[172:175], v[120:123]
	v_mfma_f32_16x16x32_bf16 v[104:107], v[88:91], v[196:199], v[104:107]
	v_mfma_f32_16x16x32_bf16 v[96:99], v[100:103], v[196:199], v[96:99]
	v_mfma_f32_16x16x32_bf16 v[76:79], v[88:91], v[204:207], v[76:79]
	v_mfma_f32_16x16x32_bf16 v[72:75], v[100:103], v[204:207], v[72:75]
	v_mfma_f32_16x16x32_bf16 v[142:145], v[92:95], v[166:169], v[142:145]
	v_mfma_f32_16x16x32_bf16 v[138:141], v[108:111], v[166:169], v[138:141]
	v_mfma_f32_16x16x32_bf16 v[124:127], v[92:95], v[188:191], v[124:127]
	v_mfma_f32_16x16x32_bf16 v[120:123], v[108:111], v[188:191], v[120:123]
	v_mfma_f32_16x16x32_bf16 v[104:107], v[92:95], v[200:203], v[104:107]
	v_mfma_f32_16x16x32_bf16 v[96:99], v[108:111], v[200:203], v[96:99]
	v_mfma_f32_16x16x32_bf16 v[76:79], v[92:95], v[208:211], v[76:79]
	v_mfma_f32_16x16x32_bf16 v[72:75], v[108:111], v[208:211], v[72:75]
	v_mfma_f32_16x16x32_bf16 v[134:137], v[146:149], v[162:165], v[134:137]
	v_mfma_f32_16x16x32_bf16 v[130:133], v[154:157], v[162:165], v[130:133]
	v_mfma_f32_16x16x32_bf16 v[116:119], v[146:149], v[172:175], v[116:119]
	v_mfma_f32_16x16x32_bf16 v[112:115], v[154:157], v[172:175], v[112:115]
	v_mfma_f32_16x16x32_bf16 v[84:87], v[146:149], v[196:199], v[84:87]
	v_mfma_f32_16x16x32_bf16 v[80:83], v[154:157], v[196:199], v[80:83]
	v_mfma_f32_16x16x32_bf16 v[68:71], v[146:149], v[204:207], v[68:71]
	v_mfma_f32_16x16x32_bf16 v[64:67], v[154:157], v[204:207], v[64:67]
	v_mfma_f32_16x16x32_bf16 v[134:137], v[150:153], v[166:169], v[134:137]
	v_mfma_f32_16x16x32_bf16 v[130:133], v[158:161], v[166:169], v[130:133]
	v_mfma_f32_16x16x32_bf16 v[116:119], v[150:153], v[188:191], v[116:119]
	v_mfma_f32_16x16x32_bf16 v[112:115], v[158:161], v[188:191], v[112:115]
	v_mfma_f32_16x16x32_bf16 v[84:87], v[150:153], v[200:203], v[84:87]
	v_mfma_f32_16x16x32_bf16 v[80:83], v[158:161], v[200:203], v[80:83]
	v_mfma_f32_16x16x32_bf16 v[68:71], v[150:153], v[208:211], v[68:71]
	v_mfma_f32_16x16x32_bf16 v[64:67], v[158:161], v[208:211], v[64:67]
	s_barrier
; #define PG8_STAGE(bufoff, gbase, voff) do { _Pragma("unroll") for (int _i = 0; _i < 2; ++_i) \
;         __builtin_amdgcn_global_load_lds((const unsigned*)((const char*)(gbase) + (voff)[_i]), (PG8_LAS unsigned*)(lds + (bufoff) + ldsw + _i * 8192), 16, 0, 0); } while (0)
; #define PG8_LDA(dst, b, h) do { _Pragma("unroll") for (int m = 0; m < 4; ++m) _Pragma("unroll") for (int k = 0; k < 2; ++k) dst[m][k] = *(const PG8_LAS bf16x8*)(lds + PG8_SA(b, h) + aoff + m * 2048 + k * 1024); } while (0)
; #define PG8_LDB(dst, b, h) do { _Pragma("unroll") for (int n = 0; n < 2; ++n) _Pragma("unroll") for (int k = 0; k < 2; ++k) dst[n][k] = *(const PG8_LAS bf16x8*)(lds + PG8_SB(b, h) + boff + n * 2048 + k * 1024); } while (0)
; #define PG8_MMA(ai, bj, At, Bt) do { __builtin_amdgcn_s_setprio(1); _Pragma("unroll") for (int m = 0; m < 4; ++m) _Pragma("unroll") for (int n = 0; n < 2; ++n) _Pragma("unroll") for (int k = 0; k < 2; ++k) \
;         acc[ai][bj][m][n] = __builtin_amdgcn_mfma_f32_16x16x32_bf16(Bt[n][k], At[m][k], acc[ai][bj][m][n], 0, 0, 0); __builtin_amdgcn_s_setprio(0); } while (0)
; #define PG8_WAIT_V(n) asm volatile("s_waitcnt vmcnt(" #n ")" ::: "memory")
; #define PG8_WAIT_L(n) asm volatile("s_waitcnt lgkmcnt(" #n ")" ::: "memory")
; #define PG8_BAR __builtin_amdgcn_s_barrier()
; #define PG8_SCHED __builtin_amdgcn_sched_barrier(0)
; template <class Epi, class Sched, bool ALIGN_EPI>
; __device__ __forceinline__ void gemm_phase(PG8_LAS unsigned char* lds, const Gemm g, const Sched& S, const Epi& E, const int tid) {
;     ...
;             PG8_LDB(B0, 0, 0); PG8_LDB(B1, 0, 1); PG8_SCHED; PG8_LDA(At, 0, 0); PG8_STAGE(PG8_SA(1, 1), a1 + hstepA, voffA);
;             PG8_WAIT_V(8); PG8_WAIT_L(0); PG8_BAR; PG8_MMA(0, 0, At, B0); PG8_MMA(0, 1, At, B1); PG8_BAR; PG8_SCHED;
;     ...
;             PG8_LDA(At, 1, 1); PG8_STAGE(PG8_SB(1, 0), b3, voffB); PG8_STAGE(PG8_SB(1, 1), b3 + hstepB, voffB); PG8_STAGE(PG8_SA(1, 0), a3, voffA);
;             PG8_WAIT_V(8); PG8_WAIT_L(0); PG8_BAR; PG8_MMA(1, 0, At, B0); PG8_MMA(1, 1, At, B1); PG8_BAR; PG8_SCHED;
	s_add_u32 s26, s24, 0x8000
	s_addc_u32 s27, s25, 0
	s_add_i32 s54, s54, s30
	s_mov_b32 m0, s54
	ds_read_b128 v[162:165], v185 offset:49152
	ds_read_b128 v[166:169], v185 offset:50176
	ds_read_b128 v[172:175], v185 offset:51200
	ds_read_b128 v[188:191], v185 offset:52224
	ds_read_b128 v[196:199], v185 offset:53248
	ds_read_b128 v[200:203], v185 offset:54272
	ds_read_b128 v[204:207], v185 offset:55296
	ds_read_b128 v[208:211], v185 offset:56320
	global_load_lds_dwordx4 v178, s[26:27]
	s_add_i32 m0, s54, 0x2000
	s_add_u32 s24, s24, 0xc000
	s_addc_u32 s25, s25, 0
	global_load_lds_dwordx4 v182, s[26:27]
	s_add_i32 s26, s55, s30
	s_mov_b32 m0, s26
	s_nop 0
	global_load_lds_dwordx4 v178, s[24:25]
	s_add_i32 m0, s26, 0x2000
	s_nop 0
	global_load_lds_dwordx4 v182, s[24:25]
	s_mov_b32 m0, s40
	s_nop 0
	global_load_lds_dwordx4 v176, s[20:21]
	s_mov_b32 m0, s41
	s_nop 0
	global_load_lds_dwordx4 v180, s[20:21]
	s_waitcnt vmcnt(8)
	s_waitcnt lgkmcnt(0)
	s_barrier
	v_mfma_f32_16x16x32_bf16 v[60:63], v[88:91], v[162:165], v[60:63]
	v_mfma_f32_16x16x32_bf16 v[56:59], v[100:103], v[162:165], v[56:59]
	v_mfma_f32_16x16x32_bf16 v[44:47], v[88:91], v[172:175], v[44:47]
	v_mfma_f32_16x16x32_bf16 v[40:43], v[100:103], v[172:175], v[40:43]
	v_mfma_f32_16x16x32_bf16 v[28:31], v[88:91], v[196:199], v[28:31]
	v_mfma_f32_16x16x32_bf16 v[24:27], v[100:103], v[196:199], v[24:27]
	v_mfma_f32_16x16x32_bf16 v[12:15], v[88:91], v[204:207], v[12:15]
	v_mfma_f32_16x16x32_bf16 v[8:11], v[100:103], v[204:207], v[8:11]
	v_mfma_f32_16x16x32_bf16 v[60:63], v[92:95], v[166:169], v[60:63]
	v_mfma_f32_16x16x32_bf16 v[56:59], v[108:111], v[166:169], v[56:59]
	v_mfma_f32_16x16x32_bf16 v[44:47], v[92:95], v[188:191], v[44:47]
	v_mfma_f32_16x16x32_bf16 v[40:43], v[108:111], v[188:191], v[40:43]
	v_mfma_f32_16x16x32_bf16 v[28:31], v[92:95], v[200:203], v[28:31]
	v_mfma_f32_16x16x32_bf16 v[24:27], v[108:111], v[200:203], v[24:27]
	v_mfma_f32_16x16x32_bf16 v[12:15], v[92:95], v[208:211], v[12:15]
	v_mfma_f32_16x16x32_bf16 v[8:11], v[108:111], v[208:211], v[8:11]
	v_mfma_f32_16x16x32_bf16 v[52:55], v[146:149], v[162:165], v[52:55]
	v_mfma_f32_16x16x32_bf16 v[48:51], v[154:157], v[162:165], v[48:51]
	v_mfma_f32_16x16x32_bf16 v[36:39], v[146:149], v[172:175], v[36:39]
	v_mfma_f32_16x16x32_bf16 v[32:35], v[154:157], v[172:175], v[32:35]
	v_mfma_f32_16x16x32_bf16 v[20:23], v[146:149], v[196:199], v[20:23]
	v_mfma_f32_16x16x32_bf16 v[16:19], v[154:157], v[196:199], v[16:19]
	v_mfma_f32_16x16x32_bf16 v[4:7], v[146:149], v[204:207], v[4:7]
	v_mfma_f32_16x16x32_bf16 v[0:3], v[154:157], v[204:207], v[0:3]
	v_mfma_f32_16x16x32_bf16 v[52:55], v[150:153], v[166:169], v[52:55]
	v_mfma_f32_16x16x32_bf16 v[48:51], v[158:161], v[166:169], v[48:51]
	v_mfma_f32_16x16x32_bf16 v[36:39], v[150:153], v[188:191], v[36:39]
	v_mfma_f32_16x16x32_bf16 v[32:35], v[158:161], v[188:191], v[32:35]
	v_mfma_f32_16x16x32_bf16 v[20:23], v[150:153], v[200:203], v[20:23]
	v_mfma_f32_16x16x32_bf16 v[16:19], v[158:161], v[200:203], v[16:19]
	v_mfma_f32_16x16x32_bf16 v[4:7], v[150:153], v[208:211], v[4:7]
	v_mfma_f32_16x16x32_bf16 v[0:3], v[158:161], v[208:211], v[0:3]
	s_barrier
	s_add_u32 s52, s52, 0x10000
	s_addc_u32 s53, s53, 0
	s_mov_b64 s[20:21], s[22:23]
.LBB0_1396:
	s_add_u32 s54, s20, 1
	s_addc_u32 s55, s21, 0
	s_add_u32 s22, s20, 2
	s_addc_u32 s23, s21, 0
	s_lshl_b64 s[24:25], s[22:23], s44
	s_add_u32 s21, s18, s24
	s_addc_u32 s24, s19, s25
	s_cmp_eq_u32 s45, s20
	s_cselect_b32 s26, s8, s21
	s_cselect_b32 s27, s9, s24
	s_cselect_b32 s24, s16, s52
	s_cselect_b32 s25, s17, s53
	s_add_u32 s20, s26, s38
	s_addc_u32 s21, s27, 0
	s_add_i32 s56, 0, 0x10000
	s_add_i32 s57, 0, 0x14000
	ds_read_b128 v[88:91], v192
	ds_read_b128 v[92:95], v192 offset:1024
	ds_read_b128 v[100:103], v192 offset:2048
	ds_read_b128 v[108:111], v192 offset:3072
	ds_read_b128 v[146:149], v192 offset:16384
	ds_read_b128 v[150:153], v192 offset:17408
	ds_read_b128 v[154:157], v192 offset:18432
	ds_read_b128 v[158:161], v192 offset:19456
	s_lshl_b64 s[54:55], s[54:55], s44
	s_add_u32 s54, s50, s54
	s_addc_u32 s55, s51, s55
	s_add_i32 m0, s31, 0xc000
	ds_read_b128 v[162:165], v185
	ds_read_b128 v[166:169], v185 offset:1024
	ds_read_b128 v[172:175], v185 offset:2048
	ds_read_b128 v[188:191], v185 offset:3072
	ds_read_b128 v[196:199], v185 offset:4096
	ds_read_b128 v[200:203], v185 offset:5120
	ds_read_b128 v[204:207], v185 offset:6144
	ds_read_b128 v[208:211], v185 offset:7168
	global_load_lds_dwordx4 v176, s[54:55]
	s_add_i32 m0, s31, 0xe000
	s_nop 0
	global_load_lds_dwordx4 v180, s[54:55]
	s_waitcnt vmcnt(8)
	s_waitcnt lgkmcnt(0)
	s_barrier
; #define PG8_STAGE(bufoff, gbase, voff) do { _Pragma("unroll") for (int _i = 0; _i < 2; ++_i) \
;         __builtin_amdgcn_global_load_lds((const unsigned*)((const char*)(gbase) + (voff)[_i]), (PG8_LAS unsigned*)(lds + (bufoff) + ldsw + _i * 8192), 16, 0, 0); } while (0)
; #define PG8_LDA(dst, b, h) do { _Pragma("unroll") for (int m = 0; m < 4; ++m) _Pragma("unroll") for (int k = 0; k < 2; ++k) dst[m][k] = *(const PG8_LAS bf16x8*)(lds + PG8_SA(b, h) + aoff + m * 2048 + k * 1024); } while (0)
; #define PG8_MMA(ai, bj, At, Bt) do { __builtin_amdgcn_s_setprio(1); _Pragma("unroll") for (int m = 0; m < 4; ++m) _Pragma("unroll") for (int n = 0; n < 2; ++n) _Pragma("unroll") for (int k = 0; k < 2; ++k) \
;         acc[ai][bj][m][n] = __builtin_amdgcn_mfma_f32_16x16x32_bf16(Bt[n][k], At[m][k], acc[ai][bj][m][n], 0, 0, 0); __builtin_amdgcn_s_setprio(0); } while (0)
; #define PG8_WAIT_V(n) asm volatile("s_waitcnt vmcnt(" #n ")" ::: "memory")
; #define PG8_WAIT_L(n) asm volatile("s_waitcnt lgkmcnt(" #n ")" ::: "memory")
; #define PG8_BAR __builtin_amdgcn_s_barrier()
; #define PG8_SCHED __builtin_amdgcn_sched_barrier(0)
; template <class Epi, class Sched, bool ALIGN_EPI>
; __device__ __forceinline__ void gemm_phase(PG8_LAS unsigned char* lds, const Gemm g, const Sched& S, const Epi& E, const int tid) {
;     ...
;             PG8_WAIT_V(8); PG8_WAIT_L(0); PG8_BAR; PG8_MMA(0, 0, At, B0); PG8_MMA(0, 1, At, B1); PG8_BAR; PG8_SCHED;
;             PG8_LDA(At, 0, 1); PG8_STAGE(PG8_SB(0, 0), b2, voffB); PG8_STAGE(PG8_SB(0, 1), b2 + hstepB, voffB); PG8_STAGE(PG8_SA(0, 0), a2, voffA);
;             PG8_WAIT_V(8); PG8_WAIT_L(0); PG8_BAR; PG8_MMA(1, 0, At, B0); PG8_MMA(1, 1, At, B1); PG8_BAR; PG8_SCHED;
	v_mfma_f32_16x16x32_bf16 v[142:145], v[88:91], v[162:165], v[142:145]
	v_mfma_f32_16x16x32_bf16 v[138:141], v[100:103], v[162:165], v[138:141]
	v_mfma_f32_16x16x32_bf16 v[124:127], v[88:91], v[172:175], v[124:127]
	v_mfma_f32_16x16x32_bf16 v[120:123], v[100:103], v[172:175], v[120:123]
	v_mfma_f32_16x16x32_bf16 v[104:107], v[88:91], v[196:199], v[104:107]
	v_mfma_f32_16x16x32_bf16 v[96:99], v[100:103], v[196:199], v[96:99]
	v_mfma_f32_16x16x32_bf16 v[76:79], v[88:91], v[204:207], v[76:79]
	v_mfma_f32_16x16x32_bf16 v[72:75], v[100:103], v[204:207], v[72:75]
	v_mfma_f32_16x16x32_bf16 v[142:145], v[92:95], v[166:169], v[142:145]
	v_mfma_f32_16x16x32_bf16 v[138:141], v[108:111], v[166:169], v[138:141]
	v_mfma_f32_16x16x32_bf16 v[124:127], v[92:95], v[188:191], v[124:127]
	v_mfma_f32_16x16x32_bf16 v[120:123], v[108:111], v[188:191], v[120:123]
	v_mfma_f32_16x16x32_bf16 v[104:107], v[92:95], v[200:203], v[104:107]
	v_mfma_f32_16x16x32_bf16 v[96:99], v[108:111], v[200:203], v[96:99]
	v_mfma_f32_16x16x32_bf16 v[76:79], v[92:95], v[208:211], v[76:79]
	v_mfma_f32_16x16x32_bf16 v[72:75], v[108:111], v[208:211], v[72:75]
	v_mfma_f32_16x16x32_bf16 v[134:137], v[146:149], v[162:165], v[134:137]
	v_mfma_f32_16x16x32_bf16 v[130:133], v[154:157], v[162:165], v[130:133]
	v_mfma_f32_16x16x32_bf16 v[116:119], v[146:149], v[172:175], v[116:119]
	v_mfma_f32_16x16x32_bf16 v[112:115], v[154:157], v[172:175], v[112:115]
	v_mfma_f32_16x16x32_bf16 v[84:87], v[146:149], v[196:199], v[84:87]
	v_mfma_f32_16x16x32_bf16 v[80:83], v[154:157], v[196:199], v[80:83]
	v_mfma_f32_16x16x32_bf16 v[68:71], v[146:149], v[204:207], v[68:71]
	v_mfma_f32_16x16x32_bf16 v[64:67], v[154:157], v[204:207], v[64:67]
	v_mfma_f32_16x16x32_bf16 v[134:137], v[150:153], v[166:169], v[134:137]
	v_mfma_f32_16x16x32_bf16 v[130:133], v[158:161], v[166:169], v[130:133]
	v_mfma_f32_16x16x32_bf16 v[116:119], v[150:153], v[188:191], v[116:119]
	v_mfma_f32_16x16x32_bf16 v[112:115], v[158:161], v[188:191], v[112:115]
	v_mfma_f32_16x16x32_bf16 v[84:87], v[150:153], v[200:203], v[84:87]
	v_mfma_f32_16x16x32_bf16 v[80:83], v[158:161], v[200:203], v[80:83]
	v_mfma_f32_16x16x32_bf16 v[68:71], v[150:153], v[208:211], v[68:71]
	v_mfma_f32_16x16x32_bf16 v[64:67], v[158:161], v[208:211], v[64:67]
	s_barrier
	s_add_i32 s54, s56, s30
	s_mov_b32 m0, s54
	ds_read_b128 v[162:165], v185 offset:16384
	ds_read_b128 v[166:169], v185 offset:17408
	ds_read_b128 v[172:175], v185 offset:18432
	ds_read_b128 v[188:191], v185 offset:19456
	ds_read_b128 v[196:199], v185 offset:20480
	ds_read_b128 v[200:203], v185 offset:21504
	ds_read_b128 v[204:207], v185 offset:22528
	ds_read_b128 v[208:211], v185 offset:23552
	global_load_lds_dwordx4 v178, s[24:25]
	s_add_i32 m0, s54, 0x2000
	s_add_u32 s54, s24, 0x4000
	s_addc_u32 s55, s25, 0
	s_add_i32 s56, s57, s30
	global_load_lds_dwordx4 v182, s[24:25]
	s_mov_b32 m0, s56
	s_nop 0
	global_load_lds_dwordx4 v178, s[54:55]
	s_add_i32 m0, s56, 0x2000
	s_nop 0
	global_load_lds_dwordx4 v182, s[54:55]
	s_mov_b32 m0, s31
	s_nop 0
	global_load_lds_dwordx4 v176, s[26:27]
	s_mov_b32 m0, s33
	s_nop 0
	global_load_lds_dwordx4 v180, s[26:27]
	s_waitcnt vmcnt(8)
	s_waitcnt lgkmcnt(0)
	s_barrier
	v_mfma_f32_16x16x32_bf16 v[60:63], v[88:91], v[162:165], v[60:63]
	v_mfma_f32_16x16x32_bf16 v[56:59], v[100:103], v[162:165], v[56:59]
	v_mfma_f32_16x16x32_bf16 v[44:47], v[88:91], v[172:175], v[44:47]
	v_mfma_f32_16x16x32_bf16 v[40:43], v[100:103], v[172:175], v[40:43]
	v_mfma_f32_16x16x32_bf16 v[28:31], v[88:91], v[196:199], v[28:31]
	v_mfma_f32_16x16x32_bf16 v[24:27], v[100:103], v[196:199], v[24:27]
	v_mfma_f32_16x16x32_bf16 v[12:15], v[88:91], v[204:207], v[12:15]
	v_mfma_f32_16x16x32_bf16 v[8:11], v[100:103], v[204:207], v[8:11]
	v_mfma_f32_16x16x32_bf16 v[60:63], v[92:95], v[166:169], v[60:63]
	v_mfma_f32_16x16x32_bf16 v[56:59], v[108:111], v[166:169], v[56:59]
	v_mfma_f32_16x16x32_bf16 v[44:47], v[92:95], v[188:191], v[44:47]
	v_mfma_f32_16x16x32_bf16 v[40:43], v[108:111], v[188:191], v[40:43]
	v_mfma_f32_16x16x32_bf16 v[28:31], v[92:95], v[200:203], v[28:31]
	v_mfma_f32_16x16x32_bf16 v[24:27], v[108:111], v[200:203], v[24:27]
	v_mfma_f32_16x16x32_bf16 v[12:15], v[92:95], v[208:211], v[12:15]
	v_mfma_f32_16x16x32_bf16 v[8:11], v[108:111], v[208:211], v[8:11]
	v_mfma_f32_16x16x32_bf16 v[52:55], v[146:149], v[162:165], v[52:55]
	v_mfma_f32_16x16x32_bf16 v[48:51], v[154:157], v[162:165], v[48:51]
	v_mfma_f32_16x16x32_bf16 v[36:39], v[146:149], v[172:175], v[36:39]
	v_mfma_f32_16x16x32_bf16 v[32:35], v[154:157], v[172:175], v[32:35]
	v_mfma_f32_16x16x32_bf16 v[20:23], v[146:149], v[196:199], v[20:23]
	v_mfma_f32_16x16x32_bf16 v[16:19], v[154:157], v[196:199], v[16:19]
	v_mfma_f32_16x16x32_bf16 v[4:7], v[146:149], v[204:207], v[4:7]
	v_mfma_f32_16x16x32_bf16 v[0:3], v[154:157], v[204:207], v[0:3]
	v_mfma_f32_16x16x32_bf16 v[52:55], v[150:153], v[166:169], v[52:55]
	v_mfma_f32_16x16x32_bf16 v[48:51], v[158:161], v[166:169], v[48:51]
	v_mfma_f32_16x16x32_bf16 v[36:39], v[150:153], v[188:191], v[36:39]
	v_mfma_f32_16x16x32_bf16 v[32:35], v[158:161], v[188:191], v[32:35]
	v_mfma_f32_16x16x32_bf16 v[20:23], v[150:153], v[200:203], v[20:23]
	v_mfma_f32_16x16x32_bf16 v[16:19], v[158:161], v[200:203], v[16:19]
	v_mfma_f32_16x16x32_bf16 v[4:7], v[150:153], v[208:211], v[4:7]
	v_mfma_f32_16x16x32_bf16 v[0:3], v[158:161], v[208:211], v[0:3]
	s_barrier
; #define PG8_STAGE(bufoff, gbase, voff) do { _Pragma("unroll") for (int _i = 0; _i < 2; ++_i) \
;         __builtin_amdgcn_global_load_lds((const unsigned*)((const char*)(gbase) + (voff)[_i]), (PG8_LAS unsigned*)(lds + (bufoff) + ldsw + _i * 8192), 16, 0, 0); } while (0)
; #define PG8_LDA(dst, b, h) do { _Pragma("unroll") for (int m = 0; m < 4; ++m) _Pragma("unroll") for (int k = 0; k < 2; ++k) dst[m][k] = *(const PG8_LAS bf16x8*)(lds + PG8_SA(b, h) + aoff + m * 2048 + k * 1024); } while (0)
; #define PG8_LDB(dst, b, h) do { _Pragma("unroll") for (int n = 0; n < 2; ++n) _Pragma("unroll") for (int k = 0; k < 2; ++k) dst[n][k] = *(const PG8_LAS bf16x8*)(lds + PG8_SB(b, h) + boff + n * 2048 + k * 1024); } while (0)
; #define PG8_MMA(ai, bj, At, Bt) do { __builtin_amdgcn_s_setprio(1); _Pragma("unroll") for (int m = 0; m < 4; ++m) _Pragma("unroll") for (int n = 0; n < 2; ++n) _Pragma("unroll") for (int k = 0; k < 2; ++k) \
;         acc[ai][bj][m][n] = __builtin_amdgcn_mfma_f32_16x16x32_bf16(Bt[n][k], At[m][k], acc[ai][bj][m][n], 0, 0, 0); __builtin_amdgcn_s_setprio(0); } while (0)
; #define PG8_WAIT_V(n) asm volatile("s_waitcnt vmcnt(" #n ")" ::: "memory")
; #define PG8_WAIT_L(n) asm volatile("s_waitcnt lgkmcnt(" #n ")" ::: "memory")
; #define PG8_BAR __builtin_amdgcn_s_barrier()
; #define PG8_SCHED __builtin_amdgcn_sched_barrier(0)
; template <class Epi, class Sched, bool ALIGN_EPI>
; __device__ __forceinline__ void gemm_phase(PG8_LAS unsigned char* lds, const Gemm g, const Sched& S, const Epi& E, const int tid) {
;     ...
;             PG8_LDB(B0, 1, 0); PG8_LDB(B1, 1, 1); PG8_SCHED; PG8_LDA(At, 1, 0); PG8_STAGE(PG8_SA(0, 1), a2 + hstepA, voffA);
;             PG8_WAIT_V(8); PG8_WAIT_L(0); PG8_BAR; PG8_MMA(0, 0, At, B0); PG8_MMA(0, 1, At, B1); PG8_BAR; PG8_SCHED;
;             PG8_LDA(At, 1, 1); PG8_STAGE(PG8_SB(1, 0), b3, voffB); PG8_STAGE(PG8_SB(1, 1), b3 + hstepB, voffB); PG8_STAGE(PG8_SA(1, 0), a3, voffA);
;             PG8_WAIT_V(8); PG8_WAIT_L(0); PG8_BAR; PG8_MMA(1, 0, At, B0); PG8_MMA(1, 1, At, B1); PG8_BAR; PG8_SCHED;
;         }
;         if constexpr (ALIGN_EPI) { if (wr == 0) PG8_BAR; }
	s_add_i32 s54, 0, 0x18000
	s_add_i32 s55, 0, 0x1c000
	ds_read_b128 v[88:91], v192 offset:32768
	ds_read_b128 v[92:95], v192 offset:33792
	ds_read_b128 v[100:103], v192 offset:34816
	ds_read_b128 v[108:111], v192 offset:35840
	ds_read_b128 v[146:149], v192 offset:49152
	ds_read_b128 v[150:153], v192 offset:50176
	ds_read_b128 v[154:157], v192 offset:51200
	ds_read_b128 v[158:161], v192 offset:52224
	s_add_u32 s26, s26, s68
	s_addc_u32 s27, s27, s69
	s_mov_b32 m0, s34
	ds_read_b128 v[162:165], v185 offset:32768
	ds_read_b128 v[166:169], v185 offset:33792
	ds_read_b128 v[172:175], v185 offset:34816
	ds_read_b128 v[188:191], v185 offset:35840
	ds_read_b128 v[196:199], v185 offset:36864
	ds_read_b128 v[200:203], v185 offset:37888
	ds_read_b128 v[204:207], v185 offset:38912
	ds_read_b128 v[208:211], v185 offset:39936
	global_load_lds_dwordx4 v176, s[26:27]
	s_mov_b32 m0, s35
	s_nop 0
	global_load_lds_dwordx4 v180, s[26:27]
	s_waitcnt vmcnt(8)
	s_waitcnt lgkmcnt(0)
	s_barrier
	v_mfma_f32_16x16x32_bf16 v[142:145], v[88:91], v[162:165], v[142:145]
	v_mfma_f32_16x16x32_bf16 v[138:141], v[100:103], v[162:165], v[138:141]
	v_mfma_f32_16x16x32_bf16 v[124:127], v[88:91], v[172:175], v[124:127]
	v_mfma_f32_16x16x32_bf16 v[120:123], v[100:103], v[172:175], v[120:123]
	v_mfma_f32_16x16x32_bf16 v[104:107], v[88:91], v[196:199], v[104:107]
	v_mfma_f32_16x16x32_bf16 v[96:99], v[100:103], v[196:199], v[96:99]
	v_mfma_f32_16x16x32_bf16 v[76:79], v[88:91], v[204:207], v[76:79]
	v_mfma_f32_16x16x32_bf16 v[72:75], v[100:103], v[204:207], v[72:75]
	v_mfma_f32_16x16x32_bf16 v[142:145], v[92:95], v[166:169], v[142:145]
	v_mfma_f32_16x16x32_bf16 v[138:141], v[108:111], v[166:169], v[138:141]
	v_mfma_f32_16x16x32_bf16 v[124:127], v[92:95], v[188:191], v[124:127]
	v_mfma_f32_16x16x32_bf16 v[120:123], v[108:111], v[188:191], v[120:123]
	v_mfma_f32_16x16x32_bf16 v[104:107], v[92:95], v[200:203], v[104:107]
	v_mfma_f32_16x16x32_bf16 v[96:99], v[108:111], v[200:203], v[96:99]
	v_mfma_f32_16x16x32_bf16 v[76:79], v[92:95], v[208:211], v[76:79]
	v_mfma_f32_16x16x32_bf16 v[72:75], v[108:111], v[208:211], v[72:75]
	v_mfma_f32_16x16x32_bf16 v[134:137], v[146:149], v[162:165], v[134:137]
	v_mfma_f32_16x16x32_bf16 v[130:133], v[154:157], v[162:165], v[130:133]
	v_mfma_f32_16x16x32_bf16 v[116:119], v[146:149], v[172:175], v[116:119]
	v_mfma_f32_16x16x32_bf16 v[112:115], v[154:157], v[172:175], v[112:115]
	v_mfma_f32_16x16x32_bf16 v[84:87], v[146:149], v[196:199], v[84:87]
	v_mfma_f32_16x16x32_bf16 v[80:83], v[154:157], v[196:199], v[80:83]
	v_mfma_f32_16x16x32_bf16 v[68:71], v[146:149], v[204:207], v[68:71]
	v_mfma_f32_16x16x32_bf16 v[64:67], v[154:157], v[204:207], v[64:67]
	v_mfma_f32_16x16x32_bf16 v[134:137], v[150:153], v[166:169], v[134:137]
	v_mfma_f32_16x16x32_bf16 v[130:133], v[158:161], v[166:169], v[130:133]
	v_mfma_f32_16x16x32_bf16 v[116:119], v[150:153], v[188:191], v[116:119]
	v_mfma_f32_16x16x32_bf16 v[112:115], v[158:161], v[188:191], v[112:115]
	v_mfma_f32_16x16x32_bf16 v[84:87], v[150:153], v[200:203], v[84:87]
	v_mfma_f32_16x16x32_bf16 v[80:83], v[158:161], v[200:203], v[80:83]
	v_mfma_f32_16x16x32_bf16 v[68:71], v[150:153], v[208:211], v[68:71]
	v_mfma_f32_16x16x32_bf16 v[64:67], v[158:161], v[208:211], v[64:67]
	s_barrier
	s_add_u32 s26, s24, 0x8000
	s_addc_u32 s27, s25, 0
	s_add_i32 s54, s54, s30
	s_mov_b32 m0, s54
	ds_read_b128 v[162:165], v185 offset:49152
	ds_read_b128 v[166:169], v185 offset:50176
	ds_read_b128 v[172:175], v185 offset:51200
	ds_read_b128 v[188:191], v185 offset:52224
	ds_read_b128 v[196:199], v185 offset:53248
	ds_read_b128 v[200:203], v185 offset:54272
	ds_read_b128 v[204:207], v185 offset:55296
	ds_read_b128 v[208:211], v185 offset:56320
	global_load_lds_dwordx4 v178, s[26:27]
	s_add_i32 m0, s54, 0x2000
	s_add_u32 s24, s24, 0xc000
	s_addc_u32 s25, s25, 0
	global_load_lds_dwordx4 v182, s[26:27]
	s_add_i32 s26, s55, s30
	s_mov_b32 m0, s26
	s_nop 0
	global_load_lds_dwordx4 v178, s[24:25]
	s_add_i32 m0, s26, 0x2000
	s_nop 0
	global_load_lds_dwordx4 v182, s[24:25]
	s_mov_b32 m0, s40
	s_nop 0
	global_load_lds_dwordx4 v176, s[20:21]
	s_mov_b32 m0, s41
	s_nop 0
	global_load_lds_dwordx4 v180, s[20:21]
	s_waitcnt vmcnt(8)
	s_waitcnt lgkmcnt(0)
	s_barrier
	v_mfma_f32_16x16x32_bf16 v[60:63], v[88:91], v[162:165], v[60:63]
	v_mfma_f32_16x16x32_bf16 v[56:59], v[100:103], v[162:165], v[56:59]
	v_mfma_f32_16x16x32_bf16 v[44:47], v[88:91], v[172:175], v[44:47]
	v_mfma_f32_16x16x32_bf16 v[40:43], v[100:103], v[172:175], v[40:43]
	v_mfma_f32_16x16x32_bf16 v[28:31], v[88:91], v[196:199], v[28:31]
	v_mfma_f32_16x16x32_bf16 v[24:27], v[100:103], v[196:199], v[24:27]
	v_mfma_f32_16x16x32_bf16 v[12:15], v[88:91], v[204:207], v[12:15]
	v_mfma_f32_16x16x32_bf16 v[8:11], v[100:103], v[204:207], v[8:11]
	v_mfma_f32_16x16x32_bf16 v[60:63], v[92:95], v[166:169], v[60:63]
	v_mfma_f32_16x16x32_bf16 v[56:59], v[108:111], v[166:169], v[56:59]
	v_mfma_f32_16x16x32_bf16 v[44:47], v[92:95], v[188:191], v[44:47]
	v_mfma_f32_16x16x32_bf16 v[40:43], v[108:111], v[188:191], v[40:43]
	v_mfma_f32_16x16x32_bf16 v[28:31], v[92:95], v[200:203], v[28:31]
	v_mfma_f32_16x16x32_bf16 v[24:27], v[108:111], v[200:203], v[24:27]
	v_mfma_f32_16x16x32_bf16 v[12:15], v[92:95], v[208:211], v[12:15]
	v_mfma_f32_16x16x32_bf16 v[8:11], v[108:111], v[208:211], v[8:11]
	v_mfma_f32_16x16x32_bf16 v[52:55], v[146:149], v[162:165], v[52:55]
	v_mfma_f32_16x16x32_bf16 v[48:51], v[154:157], v[162:165], v[48:51]
	v_mfma_f32_16x16x32_bf16 v[36:39], v[146:149], v[172:175], v[36:39]
	v_mfma_f32_16x16x32_bf16 v[32:35], v[154:157], v[172:175], v[32:35]
	v_mfma_f32_16x16x32_bf16 v[20:23], v[146:149], v[196:199], v[20:23]
	v_mfma_f32_16x16x32_bf16 v[16:19], v[154:157], v[196:199], v[16:19]
	v_mfma_f32_16x16x32_bf16 v[4:7], v[146:149], v[204:207], v[4:7]
	v_mfma_f32_16x16x32_bf16 v[0:3], v[154:157], v[204:207], v[0:3]
	v_mfma_f32_16x16x32_bf16 v[52:55], v[150:153], v[166:169], v[52:55]
	v_mfma_f32_16x16x32_bf16 v[48:51], v[158:161], v[166:169], v[48:51]
	v_mfma_f32_16x16x32_bf16 v[36:39], v[150:153], v[188:191], v[36:39]
	v_mfma_f32_16x16x32_bf16 v[32:35], v[158:161], v[188:191], v[32:35]
	v_mfma_f32_16x16x32_bf16 v[20:23], v[150:153], v[200:203], v[20:23]
	v_mfma_f32_16x16x32_bf16 v[16:19], v[158:161], v[200:203], v[16:19]
	v_mfma_f32_16x16x32_bf16 v[4:7], v[150:153], v[208:211], v[4:7]
	v_mfma_f32_16x16x32_bf16 v[0:3], v[158:161], v[208:211], v[0:3]
	s_barrier
	s_add_u32 s52, s52, 0x10000
	s_addc_u32 s53, s53, 0
	s_cmp_ge_u32 s22, s37
	s_mov_b64 s[20:21], s[22:23]
	s_cbranch_scc0 .LBB0_1396
	s_and_b64 vcc, exec, s[14:15]
	s_cbranch_vccz .LBB0_1399
	s_barrier
